# c5
# speedup vs baseline: 1.0295x; 1.0057x over previous
_Z6mxgemmILi0ELi1024ELi4EEvPKcS1_PKfS3_Pvi:
	s_load_dwordx8 s[4:11], s[0:1], 0x0
	s_load_dword s3, s[0:1], 0x28
	s_ashr_i32 s12, s2, 31
	s_lshr_b32 s12, s12, 29
	s_add_i32 s12, s2, s12
	s_ashr_i32 s13, s12, 3
	s_waitcnt lgkmcnt(0)
	s_lshl_b32 s14, s3, 3
	s_abs_i32 s15, s14
	v_cvt_f32_u32_e32 v1, s15
	s_and_b32 s12, s12, 0x3ffffff8
	s_sub_i32 s2, s2, s12
	s_mul_i32 s2, s2, s3
	v_rcp_iflag_f32_e32 v1, v1
	s_lshl_b32 s2, s2, 2
	s_add_i32 s2, s2, s13
	s_sub_i32 s13, 0, s15
	v_mul_f32_e32 v1, 0x4f7ffffe, v1
	v_cvt_u32_f32_e32 v1, v1
	s_abs_i32 s12, s2
	v_readfirstlane_b32 s33, v0
	s_xor_b32 s3, s2, s14
	v_readfirstlane_b32 s16, v1
	s_mul_i32 s13, s13, s16
	s_mul_hi_u32 s13, s16, s13
	s_add_i32 s16, s16, s13
	s_mul_hi_u32 s13, s12, s16
	s_mul_i32 s16, s13, s15
	s_sub_i32 s12, s12, s16
	s_lshr_b32 s50, s33, 6
	s_lshr_b32 s29, s33, 8
	s_ashr_i32 s3, s3, 31
	s_add_i32 s16, s13, 1
	s_sub_i32 s17, s12, s15
	s_cmp_ge_u32 s12, s15
	s_cselect_b32 s13, s16, s13
	s_cselect_b32 s12, s17, s12
	s_add_i32 s16, s13, 1
	s_cmp_ge_u32 s12, s15
	s_cselect_b32 s12, s16, s13
	s_xor_b32 s12, s12, s3
	s_sub_i32 s3, s12, s3
	s_lshl_b32 s12, s3, 3
	s_mul_i32 s3, s3, s14
	s_sub_i32 s2, s2, s3
	s_ashr_i32 s3, s2, 31
	s_lshr_b32 s3, s3, 29
	s_add_i32 s3, s2, s3
	s_ashr_i32 s14, s3, 3
	s_and_b32 s3, s3, -8
	s_sub_i32 s2, s2, s3
	s_add_i32 s2, s2, s12
	s_ashr_i32 s15, s14, 31
	s_ashr_i32 s3, s2, 31
	s_lshl_b64 s[24:25], s[14:15], 17
	s_lshl_b64 s[44:45], s[2:3], 14
	s_add_u32 s3, s6, s44
	s_addc_u32 s12, s7, s45
	s_add_u32 s16, s3, 0xc00000
	s_mul_hi_u32 s3, s33, 0xaaaaaaab
	s_addc_u32 s17, s12, 0
	s_lshr_b32 s30, s3, 8
	s_mul_i32 s12, s30, -6
	s_lshl_b32 s28, s50, 10
	s_add_i32 s12, s12, s50
	s_lshr_b32 s13, s3, 9
	s_bitcmp1_b32 s3, 8
	s_cselect_b32 s34, 0x3000, 0
	s_lshl_b32 s3, s12, 10
	s_add_i32 s12, s50, 8
	s_mul_hi_u32 s35, s12, 0x2aaaaaab
	s_mul_i32 s31, s13, 0x6000
	s_add_i32 s52, s3, s34
	s_lshl_b32 s3, s13, 15
	s_mul_i32 s13, s35, -6
	s_add_i32 s18, s52, s31
	s_add_i32 s13, s13, s12
	s_lshr_b32 s41, s35, 1
	s_bitcmp1_b32 s35, 0
	s_cselect_b32 s37, 0x3000, 0
	s_add_i32 s12, s50, 16
	s_lshl_b32 s42, s13, 10
	s_mul_hi_u32 s38, s12, 0x2aaaaaab
	s_mul_i32 s36, s41, 0x6000
	s_add_i32 s42, s42, s37
	s_mul_i32 s13, s38, -6
	s_add_i32 s20, s42, s36
	s_add_i32 s13, s13, s12
	s_lshr_b32 s43, s38, 1
	s_bitcmp1_b32 s38, 0
	s_cselect_b32 s40, 0x3000, 0
	s_lshl_b32 s51, s13, 10
	s_mul_i32 s39, s43, 0x6000
	s_add_i32 s51, s51, s40
	s_mul_i32 s26, s2, 0x60000
	s_add_i32 s22, s51, s39
	s_mul_hi_i32 s27, s2, 0x60000
	s_add_u32 s12, s6, s26
	s_addc_u32 s13, s7, s27
	s_add_u32 s46, s4, s24
	s_addc_u32 s47, s5, s25
	s_add_i32 s52, s52, s3
	s_lshl_b32 s3, s41, 13
	s_add_i32 s3, s20, s3
	s_add_i32 s58, s3, 0
	s_lshl_b32 s3, s43, 13
	v_mov_b32_e32 v2, 0
	s_add_i32 s15, s28, 0
	s_add_i32 s3, s22, s3
	v_lshlrev_b32_e32 v4, 4, v0
	v_mov_b32_e32 v5, v2
	s_mov_b32 m0, s15
	s_add_i32 s59, s3, 0
	s_lshl_b32 s3, s50, 8
	v_lshl_add_u64 v[138:139], s[46:47], 0, v[4:5]
	global_load_lds_dwordx4 v4, s[46:47]
	s_mov_b64 s[46:47], 0x2000
	s_add_i32 s53, s52, 0
	s_add_i32 s3, s3, 0
	v_and_b32_e32 v1, 63, v0
	v_lshl_add_u64 v[8:9], v[138:139], 0, s[46:47]
	s_add_i32 s46, s15, 0x8000
	s_ashr_i32 s19, s18, 31
	s_add_i32 s47, s53, 0x2000
	s_ashr_i32 s21, s20, 31
	s_add_i32 s48, s58, 0x2000
	s_ashr_i32 s23, s22, 31
	s_add_i32 s49, s59, 0x2000
	s_add_i32 s50, s3, 0x20000
	v_lshlrev_b32_e32 v6, 4, v1
	v_mov_b32_e32 v7, v2
	s_add_u32 s54, s12, s18
	s_mov_b32 m0, s46
	v_lshl_add_u64 v[140:141], s[12:13], 0, v[6:7]
	s_addc_u32 s55, s13, s19
	s_addk_i32 s53, 0x3800
	global_load_lds_dwordx4 v[8:9], off
	v_lshl_add_u64 v[8:9], v[140:141], 0, s[18:19]
	s_mov_b32 m0, s47
	v_lshl_add_u64 v[132:133], s[54:55], 0, v[6:7]
	s_add_u32 s54, s12, s20
	global_load_lds_dwordx4 v[8:9], off
	v_lshl_add_u64 v[8:9], v[140:141], 0, s[20:21]
	s_mov_b32 m0, s48
	s_addc_u32 s55, s13, s21
	global_load_lds_dwordx4 v[8:9], off
	v_lshl_add_u64 v[8:9], v[140:141], 0, s[22:23]
	s_mov_b32 m0, s49
	v_lshl_add_u64 v[134:135], s[54:55], 0, v[6:7]
	s_add_i32 s55, s58, 0x3800
	v_lshlrev_b32_e32 v130, 2, v0
	global_load_lds_dwordx4 v[8:9], off
	s_mov_b32 m0, s50
	s_mov_b64 s[56:57], 0x1800
	s_add_u32 s12, s12, s22
	global_load_lds_dword v130, s[16:17]
	v_lshl_add_u64 v[8:9], v[132:133], 0, s[56:57]
	s_mov_b32 m0, s53
	s_addc_u32 s13, s13, s23
	global_load_lds_dwordx4 v[8:9], off
	v_lshl_add_u64 v[8:9], v[134:135], 0, s[56:57]
	s_mov_b32 m0, s55
	v_lshl_add_u64 v[136:137], s[12:13], 0, v[6:7]
	global_load_lds_dwordx4 v[8:9], off
	v_lshl_add_u64 v[8:9], v[136:137], 0, s[56:57]
	s_add_i32 s56, s59, 0x3800
	s_mov_b32 m0, s56
	s_load_dwordx2 s[12:13], s[0:1], 0x20
	global_load_lds_dwordx4 v[8:9], off
	s_mov_b64 s[70:71], 0x4000
	s_add_i32 m0, s28, 0x10000
	v_lshl_add_u64 v[8:9], v[138:139], 0, s[70:71]
	global_load_lds_dwordx4 v[8:9], off
	s_mov_b64 s[70:71], 0x6000
	s_add_i32 m0, s15, 0x18000
	v_lshl_add_u64 v[8:9], v[138:139], 0, s[70:71]
	global_load_lds_dwordx4 v[8:9], off
	s_cmp_lg_u32 s29, 1
	v_mov_b32_e32 v131, v2
	s_cbranch_scc1 .LBB2_2
	s_barrier
.LBB2_2:
	s_lshl_b32 s0, s41, 15
	s_add_i32 s0, s42, s0
	s_add_i32 s41, s0, 0x2000
	s_lshl_b32 s0, s43, 15
	v_bfe_u32 v3, v0, 4, 1
	s_add_i32 s0, s51, s0
	s_add_i32 s42, s0, 0x2000
	v_and_b32_e32 v8, 15, v0
	v_lshlrev_b32_e32 v10, 8, v3
	v_lshlrev_b32_e32 v3, 9, v3
	s_and_b32 s0, s33, 0xc0
	v_lshrrev_b32_e32 v1, 5, v1
	v_or3_b32 v3, s0, v3, v8
	v_lshlrev_b32_e32 v9, 15, v1
	v_lshl_add_u32 v11, s29, 7, v10
	v_mul_u32_u24_e32 v3, 24, v3
	s_waitcnt vmcnt(5)
	v_or_b32_e32 v11, v11, v8
	v_or3_b32 v8, v10, s0, v8
	v_or_b32_e32 v3, v3, v9
	s_add_i32 s43, 0, 0x10000
	s_addk_i32 s52, 0x2000
	v_lshl_add_u32 v11, v11, 4, v9
	v_lshlrev_b32_e32 v1, 10, v1
	v_lshlrev_b32_e32 v8, 1, v8
	v_add_u32_e32 v9, s43, v3
	s_barrier
	s_barrier
	s_add_u32 s72, s4, s24
	s_addc_u32 s73, s5, s25
	s_add_u32 s72, s72, s28
	s_addc_u32 s73, s73, 0
	s_add_u32 s72, s72, 0x8000
	s_addc_u32 s73, s73, 0
	s_add_u32 s74, s72, 0x4000
	s_addc_u32 s75, s73, 0
	s_add_u32 s76, s6, s26
	s_addc_u32 s77, s7, s27
	s_add_u32 s76, s76, 0xc000
	s_addc_u32 s77, s77, 0
	s_add_u32 s78, s76, 0xc000
	s_addc_u32 s79, s77, 0
	s_add_u32 s80, s16, s3
	s_addc_u32 s81, s17, 0
	s_add_u32 s80, s80, 0x800
	s_addc_u32 s81, s81, 0
	s_add_i32 s0, s40, s39
	s_add_i32 s0, s0, s28
	s_mulk_i32 s38, 0x1800
	s_sub_i32 s0, s0, s38
	s_addk_i32 s0, 0x4000
	v_lshl_add_u64 v[6:7], s[26:27], 0, v[6:7]
	s_ashr_i32 s1, s0, 31
	v_lshl_add_u64 v[142:143], v[6:7], 0, s[0:1]
	s_add_i32 s0, s37, s36
	s_add_i32 s0, s0, s28
	s_mulk_i32 s35, 0x1800
	s_sub_i32 s0, s0, s35
	s_addk_i32 s0, 0x2000
	s_ashr_i32 s1, s0, 31
	v_lshl_add_u64 v[144:145], v[6:7], 0, s[0:1]
	s_add_i32 s0, s34, s31
	s_add_i32 s0, s0, s28
	s_mulk_i32 s30, 0x1800
	s_sub_i32 s0, s0, s30
	s_ashr_i32 s1, s0, 31
	v_lshl_add_u64 v[146:147], v[6:7], 0, s[0:1]
	s_add_u32 s0, s4, s24
	s_addc_u32 s1, s5, s25
	v_lshl_add_u64 v[4:5], s[0:1], 0, v[4:5]
	s_mov_b64 s[0:1], 0xa000
	v_add_u32_e32 v3, 0, v3
	v_add3_u32 v161, 0, v8, v1
	v_lshl_add_u64 v[148:149], v[4:5], 0, s[0:1]
	s_movk_i32 s0, 0xa000
	s_movk_i32 s4, 0xc000
	s_add_i32 s59, s43, s52
	s_add_i32 s58, s43, s41
	s_add_i32 s57, s43, s42
	s_movk_i32 s30, 0xe000
	v_add_u32_e32 v171, 0x2000, v3
	v_add_u32_e32 v167, 0x3800, v3
	v_add_u32_e32 v162, 0x2000, v9
	v_add_u32_e32 v1, 0x3800, v9
	v_add_u32_e32 v174, 0x2180, v3
	v_add_u32_e32 v173, 0x2300, v3
	v_add_u32_e32 v172, 0x2480, v3
	v_add_u32_e32 v170, 0x3980, v3
	v_add_u32_e32 v169, 0x3b00, v3
	v_add_u32_e32 v168, 0x3c80, v3
	v_add_u32_e32 v165, 0x2180, v9
	v_add_u32_e32 v164, 0x2300, v9
	v_add_u32_e32 v163, 0x2480, v9
	v_add_u32_e32 v160, 0x3980, v9
	v_add_u32_e32 v159, 0x3b00, v9
	v_add_u32_e32 v158, 0x3c80, v9
	s_mov_b32 s61, -2
	s_movk_i32 s62, 0x1000
	v_add_u32_e32 v175, 0, v11
	s_mov_b32 s1, -1
	s_add_i32 s63, s43, s28
	s_mov_b32 s5, -1
	s_add_i32 s60, s15, 0x18000
	s_mov_b64 s[24:25], 0xc000
	s_mov_b64 s[26:27], 0xc00800
	s_mov_b64 s[28:29], 0xd800
	s_add_i32 s54, s59, 0x1800
	s_add_i32 s52, s58, 0x1800
	s_add_i32 s51, s57, 0x1800
	v_add_u32_e32 v166, s43, v11
	s_mov_b32 s31, -1
	s_mov_b64 s[34:35], 0x18000
	s_mov_b64 s[36:37], 0xc01000
	s_mov_b64 s[38:39], 0x19800
	s_mov_b64 s[40:41], 0x1000
	s_mov_b64 s[42:43], 0x8000
	v_mov_b32_e32 v3, v2
	v_mov_b32_e32 v4, v2
	v_mov_b32_e32 v5, v2
	v_mov_b32_e32 v10, v2
	v_mov_b32_e32 v11, v2
	v_mov_b32_e32 v12, v2
	v_mov_b32_e32 v13, v2
	v_mov_b32_e32 v22, v2
	v_mov_b32_e32 v23, v2
	v_mov_b32_e32 v24, v2
	v_mov_b32_e32 v25, v2
	v_mov_b32_e32 v38, v2
	v_mov_b32_e32 v39, v2
	v_mov_b32_e32 v40, v2
	v_mov_b32_e32 v41, v2
	v_mov_b32_e32 v6, v2
	v_mov_b32_e32 v7, v2
	v_mov_b32_e32 v8, v2
	v_mov_b32_e32 v9, v2
	v_mov_b32_e32 v18, v2
	v_mov_b32_e32 v19, v2
	v_mov_b32_e32 v20, v2
	v_mov_b32_e32 v21, v2
	v_mov_b32_e32 v34, v2
	v_mov_b32_e32 v35, v2
	v_mov_b32_e32 v36, v2
	v_mov_b32_e32 v37, v2
	v_mov_b32_e32 v54, v2
	v_mov_b32_e32 v55, v2
	v_mov_b32_e32 v56, v2
	v_mov_b32_e32 v57, v2
	v_mov_b32_e32 v14, v2
	v_mov_b32_e32 v15, v2
	v_mov_b32_e32 v16, v2
	v_mov_b32_e32 v17, v2
	v_mov_b32_e32 v30, v2
	v_mov_b32_e32 v31, v2
	v_mov_b32_e32 v32, v2
	v_mov_b32_e32 v33, v2
	v_mov_b32_e32 v50, v2
	v_mov_b32_e32 v51, v2
	v_mov_b32_e32 v52, v2
	v_mov_b32_e32 v53, v2
	v_mov_b32_e32 v70, v2
	v_mov_b32_e32 v71, v2
	v_mov_b32_e32 v72, v2
	v_mov_b32_e32 v73, v2
	v_mov_b32_e32 v26, v2
	v_mov_b32_e32 v27, v2
	v_mov_b32_e32 v28, v2
	v_mov_b32_e32 v29, v2
	v_mov_b32_e32 v46, v2
	v_mov_b32_e32 v47, v2
	v_mov_b32_e32 v48, v2
	v_mov_b32_e32 v49, v2
	v_mov_b32_e32 v66, v2
	v_mov_b32_e32 v67, v2
	v_mov_b32_e32 v68, v2
	v_mov_b32_e32 v69, v2
	v_mov_b32_e32 v86, v2
	v_mov_b32_e32 v87, v2
	v_mov_b32_e32 v88, v2
	v_mov_b32_e32 v89, v2
	v_mov_b32_e32 v42, v2
	v_mov_b32_e32 v43, v2
	v_mov_b32_e32 v44, v2
	v_mov_b32_e32 v45, v2
	v_mov_b32_e32 v62, v2
	v_mov_b32_e32 v63, v2
	v_mov_b32_e32 v64, v2
	v_mov_b32_e32 v65, v2
	v_mov_b32_e32 v82, v2
	v_mov_b32_e32 v83, v2
	v_mov_b32_e32 v84, v2
	v_mov_b32_e32 v85, v2
	v_mov_b32_e32 v102, v2
	v_mov_b32_e32 v103, v2
	v_mov_b32_e32 v104, v2
	v_mov_b32_e32 v105, v2
	v_mov_b32_e32 v58, v2
	v_mov_b32_e32 v59, v2
	v_mov_b32_e32 v60, v2
	v_mov_b32_e32 v61, v2
	v_mov_b32_e32 v78, v2
	v_mov_b32_e32 v79, v2
	v_mov_b32_e32 v80, v2
	v_mov_b32_e32 v81, v2
	v_mov_b32_e32 v98, v2
	v_mov_b32_e32 v99, v2
	v_mov_b32_e32 v100, v2
	v_mov_b32_e32 v101, v2
	v_mov_b32_e32 v114, v2
	v_mov_b32_e32 v115, v2
	v_mov_b32_e32 v116, v2
	v_mov_b32_e32 v117, v2
	v_mov_b32_e32 v74, v2
	v_mov_b32_e32 v75, v2
	v_mov_b32_e32 v76, v2
	v_mov_b32_e32 v77, v2
	v_mov_b32_e32 v94, v2
	v_mov_b32_e32 v95, v2
	v_mov_b32_e32 v96, v2
	v_mov_b32_e32 v97, v2
	v_mov_b32_e32 v110, v2
	v_mov_b32_e32 v111, v2
	v_mov_b32_e32 v112, v2
	v_mov_b32_e32 v113, v2
	v_mov_b32_e32 v122, v2
	v_mov_b32_e32 v123, v2
	v_mov_b32_e32 v124, v2
	v_mov_b32_e32 v125, v2
	v_mov_b32_e32 v90, v2
	v_mov_b32_e32 v91, v2
	v_mov_b32_e32 v92, v2
	v_mov_b32_e32 v93, v2
	v_mov_b32_e32 v106, v2
	v_mov_b32_e32 v107, v2
	v_mov_b32_e32 v108, v2
	v_mov_b32_e32 v109, v2
	v_mov_b32_e32 v118, v2
	v_mov_b32_e32 v119, v2
	v_mov_b32_e32 v120, v2
	v_mov_b32_e32 v121, v2
	v_mov_b32_e32 v126, v2
	v_mov_b32_e32 v127, v2
	v_mov_b32_e32 v128, v2
	v_mov_b32_e32 v129, v2
	v_add_u32_e32 v176, 0x20000, v161
	v_mov_b32_e32 v177, 0x7f7f7f7f
	v_lshl_add_u64 v[150:151], s[44:45], 0, v[130:131]
	v_and_b32_e32 v142, 63, v0
	v_lshlrev_b32_e32 v150, 2, v142
	v_lshlrev_b32_e32 v142, 4, v142
	v_add_u32_e32 v143, 0x2000, v142
	v_add_u32_e32 v144, s18, v142
	v_add_u32_e32 v145, s20, v142
	v_add_u32_e32 v146, s22, v142
	v_add_u32_e32 v147, 0x1800, v144
	v_add_u32_e32 v148, 0x1800, v145
	v_add_u32_e32 v149, 0x1800, v146
	v_add_u32_e32 v151, 0x800, v150
.LBB2_3:
	s_add_i32 s44, s62, 0xfffff000
	s_and_b32 s44, s44, 0x1000
	ds_read_b128 v[202:205], v175
	ds_read_b128 v[206:209], v175 offset:256
	ds_read_b128 v[210:213], v175 offset:512
	ds_read_b128 v[214:217], v175 offset:768
	ds_read_b128 v[218:221], v175 offset:1024
	ds_read_b128 v[222:225], v175 offset:1280
	ds_read_b128 v[226:229], v175 offset:1536
	ds_read_b128 v[230:233], v175 offset:1792
	ds_read_b64 v[178:179], v171
	ds_read_b64 v[180:181], v171 offset:8
	ds_read_b64 v[182:183], v171 offset:16
	ds_read_b64 v[184:185], v174
	ds_read_b64 v[186:187], v174 offset:8
	ds_read_b64 v[188:189], v174 offset:16
	ds_read_b64 v[190:191], v173
	ds_read_b64 v[192:193], v173 offset:8
	ds_read_b64 v[194:195], v173 offset:16
	s_mov_b32 m0, s59
	ds_read_b64 v[196:197], v172
	global_load_lds_dwordx4 v144, s[76:77]
	s_mov_b32 m0, s58
	ds_read_b64 v[198:199], v172 offset:8
	global_load_lds_dwordx4 v145, s[76:77]
	s_mov_b32 m0, s57
	ds_read_b64 v[200:201], v172 offset:16
	global_load_lds_dwordx4 v146, s[76:77]
	v_add_u32_e32 v152, s44, v176
	ds_read_u16 v240, v152
	ds_read_u16 v241, v152 offset:32
	ds_read_u16 v242, v152 offset:64
	s_add_i32 s44, s62, 0xfffff800
	s_and_b32 s44, s44, 0x1800
	s_add_i32 m0, s50, s44
	ds_read_u16 v243, v152 offset:96
	global_load_lds_dword v150, s[80:81]
	s_waitcnt vmcnt(6)
	s_waitcnt lgkmcnt(0)
	s_barrier
	v_mfma_scale_f32_16x16x128_f8f6f4 v[126:129], v[202:205], v[178:183], v[126:129], v177, v240 op_sel_hi:[0,0,0] cbsz:4 blgp:2
	v_mfma_scale_f32_16x16x128_f8f6f4 v[122:125], v[206:209], v[178:183], v[122:125], v177, v240 op_sel_hi:[0,0,0] cbsz:4 blgp:2
	v_mfma_scale_f32_16x16x128_f8f6f4 v[114:117], v[210:213], v[178:183], v[114:117], v177, v240 op_sel_hi:[0,0,0] cbsz:4 blgp:2
	v_mfma_scale_f32_16x16x128_f8f6f4 v[102:105], v[214:217], v[178:183], v[102:105], v177, v240 op_sel_hi:[0,0,0] cbsz:4 blgp:2
	v_mfma_scale_f32_16x16x128_f8f6f4 v[86:89], v[218:221], v[178:183], v[86:89], v177, v240 op_sel_hi:[0,0,0] cbsz:4 blgp:2
	v_mfma_scale_f32_16x16x128_f8f6f4 v[70:73], v[222:225], v[178:183], v[70:73], v177, v240 op_sel_hi:[0,0,0] cbsz:4 blgp:2
	v_mfma_scale_f32_16x16x128_f8f6f4 v[54:57], v[226:229], v[178:183], v[54:57], v177, v240 op_sel_hi:[0,0,0] cbsz:4 blgp:2
	v_mfma_scale_f32_16x16x128_f8f6f4 v[38:41], v[230:233], v[178:183], v[38:41], v177, v240 op_sel_hi:[0,0,0] cbsz:4 blgp:2
	v_mfma_scale_f32_16x16x128_f8f6f4 v[118:121], v[202:205], v[184:189], v[118:121], v177, v241 op_sel_hi:[0,0,0] cbsz:4 blgp:2
	v_mfma_scale_f32_16x16x128_f8f6f4 v[110:113], v[206:209], v[184:189], v[110:113], v177, v241 op_sel_hi:[0,0,0] cbsz:4 blgp:2
	v_mfma_scale_f32_16x16x128_f8f6f4 v[98:101], v[210:213], v[184:189], v[98:101], v177, v241 op_sel_hi:[0,0,0] cbsz:4 blgp:2
	v_mfma_scale_f32_16x16x128_f8f6f4 v[82:85], v[214:217], v[184:189], v[82:85], v177, v241 op_sel_hi:[0,0,0] cbsz:4 blgp:2
	v_mfma_scale_f32_16x16x128_f8f6f4 v[66:69], v[218:221], v[184:189], v[66:69], v177, v241 op_sel_hi:[0,0,0] cbsz:4 blgp:2
	v_mfma_scale_f32_16x16x128_f8f6f4 v[50:53], v[222:225], v[184:189], v[50:53], v177, v241 op_sel_hi:[0,0,0] cbsz:4 blgp:2
	v_mfma_scale_f32_16x16x128_f8f6f4 v[34:37], v[226:229], v[184:189], v[34:37], v177, v241 op_sel_hi:[0,0,0] cbsz:4 blgp:2
	v_mfma_scale_f32_16x16x128_f8f6f4 v[106:109], v[202:205], v[190:195], v[106:109], v177, v242 op_sel_hi:[0,0,0] cbsz:4 blgp:2
	v_mfma_scale_f32_16x16x128_f8f6f4 v[94:97], v[206:209], v[190:195], v[94:97], v177, v242 op_sel_hi:[0,0,0] cbsz:4 blgp:2
	v_mfma_scale_f32_16x16x128_f8f6f4 v[78:81], v[210:213], v[190:195], v[78:81], v177, v242 op_sel_hi:[0,0,0] cbsz:4 blgp:2
	v_mfma_scale_f32_16x16x128_f8f6f4 v[62:65], v[214:217], v[190:195], v[62:65], v177, v242 op_sel_hi:[0,0,0] cbsz:4 blgp:2
	v_mfma_scale_f32_16x16x128_f8f6f4 v[46:49], v[218:221], v[190:195], v[46:49], v177, v242 op_sel_hi:[0,0,0] cbsz:4 blgp:2
	v_mfma_scale_f32_16x16x128_f8f6f4 v[30:33], v[222:225], v[190:195], v[30:33], v177, v242 op_sel_hi:[0,0,0] cbsz:4 blgp:2
	v_mfma_scale_f32_16x16x128_f8f6f4 v[90:93], v[202:205], v[196:201], v[90:93], v177, v243 op_sel_hi:[0,0,0] cbsz:4 blgp:2
	v_mfma_scale_f32_16x16x128_f8f6f4 v[74:77], v[206:209], v[196:201], v[74:77], v177, v243 op_sel_hi:[0,0,0] cbsz:4 blgp:2
	v_mfma_scale_f32_16x16x128_f8f6f4 v[58:61], v[210:213], v[196:201], v[58:61], v177, v243 op_sel_hi:[0,0,0] cbsz:4 blgp:2
	v_mfma_scale_f32_16x16x128_f8f6f4 v[42:45], v[214:217], v[196:201], v[42:45], v177, v243 op_sel_hi:[0,0,0] cbsz:4 blgp:2
	v_mfma_scale_f32_16x16x128_f8f6f4 v[26:29], v[218:221], v[196:201], v[26:29], v177, v243 op_sel_hi:[0,0,0] cbsz:4 blgp:2
	v_mfma_scale_f32_16x16x128_f8f6f4 v[178:181], v[230:233], v[184:189], v[22:25], v177, v241 op_sel_hi:[0,0,0] cbsz:4 blgp:2
	v_mfma_scale_f32_16x16x128_f8f6f4 v[182:185], v[226:229], v[190:195], v[18:21], v177, v242 op_sel_hi:[0,0,0] cbsz:4 blgp:2
	v_mfma_scale_f32_16x16x128_f8f6f4 v[186:189], v[230:233], v[190:195], v[10:13], v177, v242 op_sel_hi:[0,0,0] cbsz:4 blgp:2
	v_mfma_scale_f32_16x16x128_f8f6f4 v[190:193], v[222:225], v[196:201], v[14:17], v177, v243 op_sel_hi:[0,0,0] cbsz:4 blgp:2
	v_mfma_scale_f32_16x16x128_f8f6f4 v[234:237], v[226:229], v[196:201], v[6:9], v177, v243 op_sel_hi:[0,0,0] cbsz:4 blgp:2
	v_mfma_scale_f32_16x16x128_f8f6f4 v[194:197], v[230:233], v[196:201], v[2:5], v177, v243 op_sel_hi:[0,0,0] cbsz:4 blgp:2
	s_barrier
	ds_read_b64 v[2:3], v167
	ds_read_b64 v[4:5], v167 offset:8
	ds_read_b64 v[6:7], v167 offset:16
	ds_read_b64 v[8:9], v170
	ds_read_b64 v[10:11], v170 offset:8
	ds_read_b64 v[12:13], v170 offset:16
	ds_read_b64 v[14:15], v169
	s_mov_b32 m0, s54
	ds_read_b64 v[16:17], v169 offset:8
	global_load_lds_dwordx4 v147, s[76:77]
	s_mov_b32 m0, s52
	ds_read_b64 v[18:19], v169 offset:16
	global_load_lds_dwordx4 v148, s[76:77]
	s_mov_b32 m0, s51
	ds_read_b64 v[20:21], v168
	global_load_lds_dwordx4 v149, s[76:77]
	s_mov_b32 m0, s15
	ds_read_b64 v[22:23], v168 offset:8
	global_load_lds_dwordx4 v142, s[72:73]
	s_mov_b32 m0, s46
	ds_read_b64 v[24:25], v168 offset:16
	global_load_lds_dwordx4 v143, s[72:73]
	s_waitcnt vmcnt(5)
	s_waitcnt lgkmcnt(0)
	s_barrier
	v_mfma_scale_f32_16x16x128_f8f6f4 v[126:129], v[202:205], v[2:7], v[126:129], v177, v240 op_sel:[0,1,0] op_sel_hi:[0,0,0] cbsz:4 blgp:2
	v_mfma_scale_f32_16x16x128_f8f6f4 v[122:125], v[206:209], v[2:7], v[122:125], v177, v240 op_sel:[0,1,0] op_sel_hi:[0,0,0] cbsz:4 blgp:2
	v_mfma_scale_f32_16x16x128_f8f6f4 v[114:117], v[210:213], v[2:7], v[114:117], v177, v240 op_sel:[0,1,0] op_sel_hi:[0,0,0] cbsz:4 blgp:2
	v_mfma_scale_f32_16x16x128_f8f6f4 v[102:105], v[214:217], v[2:7], v[102:105], v177, v240 op_sel:[0,1,0] op_sel_hi:[0,0,0] cbsz:4 blgp:2
	v_mfma_scale_f32_16x16x128_f8f6f4 v[86:89], v[218:221], v[2:7], v[86:89], v177, v240 op_sel:[0,1,0] op_sel_hi:[0,0,0] cbsz:4 blgp:2
	v_mfma_scale_f32_16x16x128_f8f6f4 v[70:73], v[222:225], v[2:7], v[70:73], v177, v240 op_sel:[0,1,0] op_sel_hi:[0,0,0] cbsz:4 blgp:2
	v_mfma_scale_f32_16x16x128_f8f6f4 v[54:57], v[226:229], v[2:7], v[54:57], v177, v240 op_sel:[0,1,0] op_sel_hi:[0,0,0] cbsz:4 blgp:2
	v_mfma_scale_f32_16x16x128_f8f6f4 v[38:41], v[230:233], v[2:7], v[38:41], v177, v240 op_sel:[0,1,0] op_sel_hi:[0,0,0] cbsz:4 blgp:2
	v_mfma_scale_f32_16x16x128_f8f6f4 v[118:121], v[202:205], v[8:13], v[118:121], v177, v241 op_sel:[0,1,0] op_sel_hi:[0,0,0] cbsz:4 blgp:2
	v_mfma_scale_f32_16x16x128_f8f6f4 v[110:113], v[206:209], v[8:13], v[110:113], v177, v241 op_sel:[0,1,0] op_sel_hi:[0,0,0] cbsz:4 blgp:2
	v_mfma_scale_f32_16x16x128_f8f6f4 v[98:101], v[210:213], v[8:13], v[98:101], v177, v241 op_sel:[0,1,0] op_sel_hi:[0,0,0] cbsz:4 blgp:2
	v_mfma_scale_f32_16x16x128_f8f6f4 v[82:85], v[214:217], v[8:13], v[82:85], v177, v241 op_sel:[0,1,0] op_sel_hi:[0,0,0] cbsz:4 blgp:2
	v_mfma_scale_f32_16x16x128_f8f6f4 v[66:69], v[218:221], v[8:13], v[66:69], v177, v241 op_sel:[0,1,0] op_sel_hi:[0,0,0] cbsz:4 blgp:2
	v_mfma_scale_f32_16x16x128_f8f6f4 v[50:53], v[222:225], v[8:13], v[50:53], v177, v241 op_sel:[0,1,0] op_sel_hi:[0,0,0] cbsz:4 blgp:2
	v_mfma_scale_f32_16x16x128_f8f6f4 v[34:37], v[226:229], v[8:13], v[34:37], v177, v241 op_sel:[0,1,0] op_sel_hi:[0,0,0] cbsz:4 blgp:2
	v_mfma_scale_f32_16x16x128_f8f6f4 v[106:109], v[202:205], v[14:19], v[106:109], v177, v242 op_sel:[0,1,0] op_sel_hi:[0,0,0] cbsz:4 blgp:2
	v_mfma_scale_f32_16x16x128_f8f6f4 v[94:97], v[206:209], v[14:19], v[94:97], v177, v242 op_sel:[0,1,0] op_sel_hi:[0,0,0] cbsz:4 blgp:2
	v_mfma_scale_f32_16x16x128_f8f6f4 v[78:81], v[210:213], v[14:19], v[78:81], v177, v242 op_sel:[0,1,0] op_sel_hi:[0,0,0] cbsz:4 blgp:2
	v_mfma_scale_f32_16x16x128_f8f6f4 v[62:65], v[214:217], v[14:19], v[62:65], v177, v242 op_sel:[0,1,0] op_sel_hi:[0,0,0] cbsz:4 blgp:2
	v_mfma_scale_f32_16x16x128_f8f6f4 v[46:49], v[218:221], v[14:19], v[46:49], v177, v242 op_sel:[0,1,0] op_sel_hi:[0,0,0] cbsz:4 blgp:2
	v_mfma_scale_f32_16x16x128_f8f6f4 v[30:33], v[222:225], v[14:19], v[30:33], v177, v242 op_sel:[0,1,0] op_sel_hi:[0,0,0] cbsz:4 blgp:2
	v_mfma_scale_f32_16x16x128_f8f6f4 v[90:93], v[202:205], v[20:25], v[90:93], v177, v243 op_sel:[0,1,0] op_sel_hi:[0,0,0] cbsz:4 blgp:2
	v_mfma_scale_f32_16x16x128_f8f6f4 v[74:77], v[206:209], v[20:25], v[74:77], v177, v243 op_sel:[0,1,0] op_sel_hi:[0,0,0] cbsz:4 blgp:2
	v_mfma_scale_f32_16x16x128_f8f6f4 v[58:61], v[210:213], v[20:25], v[58:61], v177, v243 op_sel:[0,1,0] op_sel_hi:[0,0,0] cbsz:4 blgp:2
	v_mfma_scale_f32_16x16x128_f8f6f4 v[42:45], v[214:217], v[20:25], v[42:45], v177, v243 op_sel:[0,1,0] op_sel_hi:[0,0,0] cbsz:4 blgp:2
	v_mfma_scale_f32_16x16x128_f8f6f4 v[26:29], v[218:221], v[20:25], v[26:29], v177, v243 op_sel:[0,1,0] op_sel_hi:[0,0,0] cbsz:4 blgp:2
	v_mfma_scale_f32_16x16x128_f8f6f4 v[178:181], v[230:233], v[8:13], v[178:181], v177, v241 op_sel:[0,1,0] op_sel_hi:[0,0,0] cbsz:4 blgp:2
	v_mfma_scale_f32_16x16x128_f8f6f4 v[182:185], v[226:229], v[14:19], v[182:185], v177, v242 op_sel:[0,1,0] op_sel_hi:[0,0,0] cbsz:4 blgp:2
	v_mfma_scale_f32_16x16x128_f8f6f4 v[186:189], v[230:233], v[14:19], v[186:189], v177, v242 op_sel:[0,1,0] op_sel_hi:[0,0,0] cbsz:4 blgp:2
	v_mfma_scale_f32_16x16x128_f8f6f4 v[190:193], v[222:225], v[20:25], v[190:193], v177, v243 op_sel:[0,1,0] op_sel_hi:[0,0,0] cbsz:4 blgp:2
	v_mfma_scale_f32_16x16x128_f8f6f4 v[198:201], v[226:229], v[20:25], v[234:237], v177, v243 op_sel:[0,1,0] op_sel_hi:[0,0,0] cbsz:4 blgp:2
	v_mfma_scale_f32_16x16x128_f8f6f4 v[194:197], v[230:233], v[20:25], v[194:197], v177, v243 op_sel:[0,1,0] op_sel_hi:[0,0,0] cbsz:4 blgp:2
	s_barrier
	ds_read_b128 v[202:205], v166
	ds_read_b128 v[206:209], v166 offset:256
	ds_read_b128 v[210:213], v166 offset:512
	ds_read_b128 v[214:217], v166 offset:768
	ds_read_b128 v[218:221], v166 offset:1024
	ds_read_b128 v[222:225], v166 offset:1280
	ds_read_b128 v[226:229], v166 offset:1536
	ds_read_b128 v[230:233], v166 offset:1792
	ds_read_b64 v[2:3], v162
	ds_read_b64 v[4:5], v162 offset:8
	ds_read_b64 v[6:7], v162 offset:16
	ds_read_b64 v[8:9], v165
	ds_read_b64 v[10:11], v165 offset:8
	ds_read_b64 v[12:13], v165 offset:16
	ds_read_b64 v[14:15], v164
	ds_read_b64 v[16:17], v164 offset:8
	ds_read_b64 v[18:19], v164 offset:16
	s_mov_b32 m0, s47
	ds_read_b64 v[20:21], v163
	global_load_lds_dwordx4 v144, s[78:79]
	s_mov_b32 m0, s48
	ds_read_b64 v[22:23], v163 offset:8
	global_load_lds_dwordx4 v145, s[78:79]
	s_mov_b32 m0, s49
	ds_read_b64 v[24:25], v163 offset:16
	global_load_lds_dwordx4 v146, s[78:79]
	v_add_u32_e32 v234, s44, v176
	ds_read_u16 v242, v234
	ds_read_u16 v243, v234 offset:32
	ds_read_u16 v244, v234 offset:64
	s_and_b32 s44, s62, 0x1000
	s_add_i32 m0, s50, s44
	ds_read_u16 v245, v234 offset:96
	global_load_lds_dword v151, s[80:81]
	s_waitcnt vmcnt(6)
	s_waitcnt lgkmcnt(0)
	s_barrier
	v_mfma_scale_f32_16x16x128_f8f6f4 v[126:129], v[202:205], v[2:7], v[126:129], v177, v242 op_sel_hi:[0,0,0] cbsz:4 blgp:2
	v_mfma_scale_f32_16x16x128_f8f6f4 v[122:125], v[206:209], v[2:7], v[122:125], v177, v242 op_sel_hi:[0,0,0] cbsz:4 blgp:2
	v_mfma_scale_f32_16x16x128_f8f6f4 v[114:117], v[210:213], v[2:7], v[114:117], v177, v242 op_sel_hi:[0,0,0] cbsz:4 blgp:2
	v_mfma_scale_f32_16x16x128_f8f6f4 v[102:105], v[214:217], v[2:7], v[102:105], v177, v242 op_sel_hi:[0,0,0] cbsz:4 blgp:2
	v_mfma_scale_f32_16x16x128_f8f6f4 v[86:89], v[218:221], v[2:7], v[86:89], v177, v242 op_sel_hi:[0,0,0] cbsz:4 blgp:2
	v_mfma_scale_f32_16x16x128_f8f6f4 v[70:73], v[222:225], v[2:7], v[70:73], v177, v242 op_sel_hi:[0,0,0] cbsz:4 blgp:2
	v_mfma_scale_f32_16x16x128_f8f6f4 v[54:57], v[226:229], v[2:7], v[54:57], v177, v242 op_sel_hi:[0,0,0] cbsz:4 blgp:2
	v_mfma_scale_f32_16x16x128_f8f6f4 v[38:41], v[230:233], v[2:7], v[38:41], v177, v242 op_sel_hi:[0,0,0] cbsz:4 blgp:2
	v_mfma_scale_f32_16x16x128_f8f6f4 v[118:121], v[202:205], v[8:13], v[118:121], v177, v243 op_sel_hi:[0,0,0] cbsz:4 blgp:2
	v_mfma_scale_f32_16x16x128_f8f6f4 v[110:113], v[206:209], v[8:13], v[110:113], v177, v243 op_sel_hi:[0,0,0] cbsz:4 blgp:2
	v_mfma_scale_f32_16x16x128_f8f6f4 v[98:101], v[210:213], v[8:13], v[98:101], v177, v243 op_sel_hi:[0,0,0] cbsz:4 blgp:2
	v_mfma_scale_f32_16x16x128_f8f6f4 v[82:85], v[214:217], v[8:13], v[82:85], v177, v243 op_sel_hi:[0,0,0] cbsz:4 blgp:2
	v_mfma_scale_f32_16x16x128_f8f6f4 v[66:69], v[218:221], v[8:13], v[66:69], v177, v243 op_sel_hi:[0,0,0] cbsz:4 blgp:2
	v_mfma_scale_f32_16x16x128_f8f6f4 v[50:53], v[222:225], v[8:13], v[50:53], v177, v243 op_sel_hi:[0,0,0] cbsz:4 blgp:2
	v_mfma_scale_f32_16x16x128_f8f6f4 v[34:37], v[226:229], v[8:13], v[34:37], v177, v243 op_sel_hi:[0,0,0] cbsz:4 blgp:2
	v_mfma_scale_f32_16x16x128_f8f6f4 v[106:109], v[202:205], v[14:19], v[106:109], v177, v244 op_sel_hi:[0,0,0] cbsz:4 blgp:2
	v_mfma_scale_f32_16x16x128_f8f6f4 v[94:97], v[206:209], v[14:19], v[94:97], v177, v244 op_sel_hi:[0,0,0] cbsz:4 blgp:2
	v_mfma_scale_f32_16x16x128_f8f6f4 v[78:81], v[210:213], v[14:19], v[78:81], v177, v244 op_sel_hi:[0,0,0] cbsz:4 blgp:2
	v_mfma_scale_f32_16x16x128_f8f6f4 v[62:65], v[214:217], v[14:19], v[62:65], v177, v244 op_sel_hi:[0,0,0] cbsz:4 blgp:2
	v_mfma_scale_f32_16x16x128_f8f6f4 v[46:49], v[218:221], v[14:19], v[46:49], v177, v244 op_sel_hi:[0,0,0] cbsz:4 blgp:2
	v_mfma_scale_f32_16x16x128_f8f6f4 v[30:33], v[222:225], v[14:19], v[30:33], v177, v244 op_sel_hi:[0,0,0] cbsz:4 blgp:2
	v_mfma_scale_f32_16x16x128_f8f6f4 v[238:241], v[226:229], v[14:19], v[182:185], v177, v244 op_sel_hi:[0,0,0] cbsz:4 blgp:2
	v_mfma_scale_f32_16x16x128_f8f6f4 v[14:17], v[230:233], v[14:19], v[186:189], v177, v244 op_sel_hi:[0,0,0] cbsz:4 blgp:2
	v_mfma_scale_f32_16x16x128_f8f6f4 v[90:93], v[202:205], v[20:25], v[90:93], v177, v245 op_sel_hi:[0,0,0] cbsz:4 blgp:2
	v_mfma_scale_f32_16x16x128_f8f6f4 v[74:77], v[206:209], v[20:25], v[74:77], v177, v245 op_sel_hi:[0,0,0] cbsz:4 blgp:2
	v_mfma_scale_f32_16x16x128_f8f6f4 v[58:61], v[210:213], v[20:25], v[58:61], v177, v245 op_sel_hi:[0,0,0] cbsz:4 blgp:2
	v_mfma_scale_f32_16x16x128_f8f6f4 v[42:45], v[214:217], v[20:25], v[42:45], v177, v245 op_sel_hi:[0,0,0] cbsz:4 blgp:2
	v_mfma_scale_f32_16x16x128_f8f6f4 v[26:29], v[218:221], v[20:25], v[26:29], v177, v245 op_sel_hi:[0,0,0] cbsz:4 blgp:2
	v_mfma_scale_f32_16x16x128_f8f6f4 v[234:237], v[230:233], v[8:13], v[178:181], v177, v243 op_sel_hi:[0,0,0] cbsz:4 blgp:2
	v_mfma_scale_f32_16x16x128_f8f6f4 v[190:193], v[222:225], v[20:25], v[190:193], v177, v245 op_sel_hi:[0,0,0] cbsz:4 blgp:2
	v_mfma_scale_f32_16x16x128_f8f6f4 v[198:201], v[226:229], v[20:25], v[198:201], v177, v245 op_sel_hi:[0,0,0] cbsz:4 blgp:2
	v_mfma_scale_f32_16x16x128_f8f6f4 v[194:197], v[230:233], v[20:25], v[194:197], v177, v245 op_sel_hi:[0,0,0] cbsz:4 blgp:2
	s_barrier
	ds_read_b64 v[2:3], v1
	ds_read_b64 v[4:5], v1 offset:8
	ds_read_b64 v[6:7], v1 offset:16
	ds_read_b64 v[8:9], v160
	ds_read_b64 v[10:11], v160 offset:8
	ds_read_b64 v[12:13], v160 offset:16
	ds_read_b64 v[178:179], v159
	s_mov_b32 m0, s53
	ds_read_b64 v[180:181], v159 offset:8
	global_load_lds_dwordx4 v147, s[78:79]
	s_mov_b32 m0, s55
	ds_read_b64 v[182:183], v159 offset:16
	global_load_lds_dwordx4 v148, s[78:79]
	s_mov_b32 m0, s56
	ds_read_b64 v[184:185], v158
	global_load_lds_dwordx4 v149, s[78:79]
	s_mov_b32 m0, s63
	ds_read_b64 v[186:187], v158 offset:8
	global_load_lds_dwordx4 v142, s[74:75]
	s_mov_b32 m0, s60
	ds_read_b64 v[188:189], v158 offset:16
	global_load_lds_dwordx4 v143, s[74:75]
	s_waitcnt vmcnt(5)
	s_waitcnt lgkmcnt(0)
	s_barrier
	v_mfma_scale_f32_16x16x128_f8f6f4 v[126:129], v[202:205], v[2:7], v[126:129], v177, v242 op_sel:[0,1,0] op_sel_hi:[0,0,0] cbsz:4 blgp:2
	v_mfma_scale_f32_16x16x128_f8f6f4 v[122:125], v[206:209], v[2:7], v[122:125], v177, v242 op_sel:[0,1,0] op_sel_hi:[0,0,0] cbsz:4 blgp:2
	v_mfma_scale_f32_16x16x128_f8f6f4 v[114:117], v[210:213], v[2:7], v[114:117], v177, v242 op_sel:[0,1,0] op_sel_hi:[0,0,0] cbsz:4 blgp:2
	v_mfma_scale_f32_16x16x128_f8f6f4 v[102:105], v[214:217], v[2:7], v[102:105], v177, v242 op_sel:[0,1,0] op_sel_hi:[0,0,0] cbsz:4 blgp:2
	v_mfma_scale_f32_16x16x128_f8f6f4 v[86:89], v[218:221], v[2:7], v[86:89], v177, v242 op_sel:[0,1,0] op_sel_hi:[0,0,0] cbsz:4 blgp:2
	v_mfma_scale_f32_16x16x128_f8f6f4 v[70:73], v[222:225], v[2:7], v[70:73], v177, v242 op_sel:[0,1,0] op_sel_hi:[0,0,0] cbsz:4 blgp:2
	v_mfma_scale_f32_16x16x128_f8f6f4 v[54:57], v[226:229], v[2:7], v[54:57], v177, v242 op_sel:[0,1,0] op_sel_hi:[0,0,0] cbsz:4 blgp:2
	v_mfma_scale_f32_16x16x128_f8f6f4 v[38:41], v[230:233], v[2:7], v[38:41], v177, v242 op_sel:[0,1,0] op_sel_hi:[0,0,0] cbsz:4 blgp:2
	v_mfma_scale_f32_16x16x128_f8f6f4 v[118:121], v[202:205], v[8:13], v[118:121], v177, v243 op_sel:[0,1,0] op_sel_hi:[0,0,0] cbsz:4 blgp:2
	v_mfma_scale_f32_16x16x128_f8f6f4 v[110:113], v[206:209], v[8:13], v[110:113], v177, v243 op_sel:[0,1,0] op_sel_hi:[0,0,0] cbsz:4 blgp:2
	v_mfma_scale_f32_16x16x128_f8f6f4 v[98:101], v[210:213], v[8:13], v[98:101], v177, v243 op_sel:[0,1,0] op_sel_hi:[0,0,0] cbsz:4 blgp:2
	v_mfma_scale_f32_16x16x128_f8f6f4 v[82:85], v[214:217], v[8:13], v[82:85], v177, v243 op_sel:[0,1,0] op_sel_hi:[0,0,0] cbsz:4 blgp:2
	v_mfma_scale_f32_16x16x128_f8f6f4 v[66:69], v[218:221], v[8:13], v[66:69], v177, v243 op_sel:[0,1,0] op_sel_hi:[0,0,0] cbsz:4 blgp:2
	v_mfma_scale_f32_16x16x128_f8f6f4 v[50:53], v[222:225], v[8:13], v[50:53], v177, v243 op_sel:[0,1,0] op_sel_hi:[0,0,0] cbsz:4 blgp:2
	v_mfma_scale_f32_16x16x128_f8f6f4 v[34:37], v[226:229], v[8:13], v[34:37], v177, v243 op_sel:[0,1,0] op_sel_hi:[0,0,0] cbsz:4 blgp:2
	v_mfma_scale_f32_16x16x128_f8f6f4 v[22:25], v[230:233], v[8:13], v[234:237], v177, v243 op_sel:[0,1,0] op_sel_hi:[0,0,0] cbsz:4 blgp:2
	v_mfma_scale_f32_16x16x128_f8f6f4 v[106:109], v[202:205], v[178:183], v[106:109], v177, v244 op_sel:[0,1,0] op_sel_hi:[0,0,0] cbsz:4 blgp:2
	v_mfma_scale_f32_16x16x128_f8f6f4 v[94:97], v[206:209], v[178:183], v[94:97], v177, v244 op_sel:[0,1,0] op_sel_hi:[0,0,0] cbsz:4 blgp:2
	v_mfma_scale_f32_16x16x128_f8f6f4 v[78:81], v[210:213], v[178:183], v[78:81], v177, v244 op_sel:[0,1,0] op_sel_hi:[0,0,0] cbsz:4 blgp:2
	v_mfma_scale_f32_16x16x128_f8f6f4 v[62:65], v[214:217], v[178:183], v[62:65], v177, v244 op_sel:[0,1,0] op_sel_hi:[0,0,0] cbsz:4 blgp:2
	v_mfma_scale_f32_16x16x128_f8f6f4 v[46:49], v[218:221], v[178:183], v[46:49], v177, v244 op_sel:[0,1,0] op_sel_hi:[0,0,0] cbsz:4 blgp:2
	v_mfma_scale_f32_16x16x128_f8f6f4 v[30:33], v[222:225], v[178:183], v[30:33], v177, v244 op_sel:[0,1,0] op_sel_hi:[0,0,0] cbsz:4 blgp:2
	v_mfma_scale_f32_16x16x128_f8f6f4 v[18:21], v[226:229], v[178:183], v[238:241], v177, v244 op_sel:[0,1,0] op_sel_hi:[0,0,0] cbsz:4 blgp:2
	v_mfma_scale_f32_16x16x128_f8f6f4 v[10:13], v[230:233], v[178:183], v[14:17], v177, v244 op_sel:[0,1,0] op_sel_hi:[0,0,0] cbsz:4 blgp:2
	v_mfma_scale_f32_16x16x128_f8f6f4 v[90:93], v[202:205], v[184:189], v[90:93], v177, v245 op_sel:[0,1,0] op_sel_hi:[0,0,0] cbsz:4 blgp:2
	v_mfma_scale_f32_16x16x128_f8f6f4 v[74:77], v[206:209], v[184:189], v[74:77], v177, v245 op_sel:[0,1,0] op_sel_hi:[0,0,0] cbsz:4 blgp:2
	v_mfma_scale_f32_16x16x128_f8f6f4 v[58:61], v[210:213], v[184:189], v[58:61], v177, v245 op_sel:[0,1,0] op_sel_hi:[0,0,0] cbsz:4 blgp:2
	v_mfma_scale_f32_16x16x128_f8f6f4 v[42:45], v[214:217], v[184:189], v[42:45], v177, v245 op_sel:[0,1,0] op_sel_hi:[0,0,0] cbsz:4 blgp:2
	v_mfma_scale_f32_16x16x128_f8f6f4 v[26:29], v[218:221], v[184:189], v[26:29], v177, v245 op_sel:[0,1,0] op_sel_hi:[0,0,0] cbsz:4 blgp:2
	v_mfma_scale_f32_16x16x128_f8f6f4 v[14:17], v[222:225], v[184:189], v[190:193], v177, v245 op_sel:[0,1,0] op_sel_hi:[0,0,0] cbsz:4 blgp:2
	v_mfma_scale_f32_16x16x128_f8f6f4 v[6:9], v[226:229], v[184:189], v[198:201], v177, v245 op_sel:[0,1,0] op_sel_hi:[0,0,0] cbsz:4 blgp:2
	v_mfma_scale_f32_16x16x128_f8f6f4 v[2:5], v[230:233], v[184:189], v[194:197], v177, v245 op_sel:[0,1,0] op_sel_hi:[0,0,0] cbsz:4 blgp:2
	s_barrier
	s_add_i32 s61, s61, 2
	s_addk_i32 s62, 0x1000
	s_add_u32 s72, s72, 0x8000
	s_addc_u32 s73, s73, 0
	s_add_u32 s74, s74, 0x8000
	s_addc_u32 s75, s75, 0
	s_add_u32 s76, s76, 0x18000
	s_addc_u32 s77, s77, 0
	s_add_u32 s78, s78, 0x18000
	s_addc_u32 s79, s79, 0
	s_add_u32 s80, s80, 0x1000
	s_addc_u32 s81, s81, 0
	s_cmp_lt_u32 s61, 4
	s_cbranch_scc1 .LBB2_3
	ds_read_b128 v[154:157], v175
	ds_read_b128 v[186:189], v175 offset:256
	ds_read_b128 v[190:193], v175 offset:512
	ds_read_b128 v[194:197], v175 offset:768
	ds_read_b128 v[198:201], v175 offset:1024
	ds_read_b128 v[202:205], v175 offset:1280
	ds_read_b128 v[206:209], v175 offset:1536
	ds_read_b128 v[210:213], v175 offset:1792
	ds_read_b64 v[142:143], v171
	ds_read_b64 v[144:145], v171 offset:8
	ds_read_b64 v[146:147], v171 offset:16
	ds_read_b64 v[148:149], v174
	ds_read_b64 v[150:151], v174 offset:8
	ds_read_b64 v[152:153], v174 offset:16
	ds_read_b64 v[174:175], v173
	ds_read_b64 v[176:177], v173 offset:8
	ds_read_b64 v[178:179], v173 offset:16
	ds_read_b64 v[180:181], v172
	ds_read_b64 v[182:183], v172 offset:8
	ds_read_b64 v[184:185], v172 offset:16
	v_add_u32_e32 v171, 0x21000, v161
	v_add_u32_e32 v172, 0x21020, v161
	v_add_u32_e32 v173, 0x21040, v161
	v_add_u32_e32 v214, 0x21060, v161
	s_mov_b64 s[0:1], 0x1c000
	s_mov_b32 m0, s63
	ds_read_u16 v171, v171
	ds_read_u16 v215, v172
	ds_read_u16 v216, v173
	ds_read_u16 v214, v214
	v_lshl_add_u64 v[172:173], v[138:139], 0, s[0:1]
	s_mov_b64 s[0:1], 0x1e000
	v_lshl_add_u64 v[138:139], v[138:139], 0, s[0:1]
	s_mov_b32 m0, s60
	s_mov_b64 s[0:1], 0x54000
	v_lshl_add_u64 v[138:139], v[140:141], 0, s[0:1]
	v_lshl_add_u64 v[140:141], v[138:139], 0, s[18:19]
	s_mov_b32 m0, s59
	v_lshl_add_u64 v[130:131], s[16:17], 0, v[130:131]
	global_load_lds_dwordx4 v[140:141], off
	v_lshl_add_u64 v[140:141], v[138:139], 0, s[20:21]
	s_mov_b32 m0, s58
	v_lshl_add_u64 v[138:139], v[138:139], 0, s[22:23]
	global_load_lds_dwordx4 v[140:141], off
	s_mov_b32 m0, s57
	s_mov_b64 s[0:1], 0x3800
	global_load_lds_dwordx4 v[138:139], off
	v_lshl_add_u64 v[130:131], v[130:131], 0, s[0:1]
	s_add_i32 m0, s3, 0x21800
	s_waitcnt lgkmcnt(0)
	v_mov_b32_e32 v172, v216
	global_load_lds_dword v[130:131], off
	s_waitcnt vmcnt(6)
	s_waitcnt lgkmcnt(0)
	v_mov_b32_e32 v130, v171
	v_mov_b32_e32 v131, v215
	v_mov_b32_e32 v217, v214
	s_barrier
	v_mov_b32_e32 v240, 0x7f7f7f7f
	s_nop 1
	v_mfma_scale_f32_16x16x128_f8f6f4 v[126:129], v[154:157], v[142:147], v[126:129], v240, v130 op_sel_hi:[0,0,0] cbsz:4 blgp:2
	v_mfma_scale_f32_16x16x128_f8f6f4 v[122:125], v[186:189], v[142:147], v[122:125], v240, v130 op_sel_hi:[0,0,0] cbsz:4 blgp:2
	v_mfma_scale_f32_16x16x128_f8f6f4 v[114:117], v[190:193], v[142:147], v[114:117], v240, v130 op_sel_hi:[0,0,0] cbsz:4 blgp:2
	v_mfma_scale_f32_16x16x128_f8f6f4 v[102:105], v[194:197], v[142:147], v[102:105], v240, v130 op_sel_hi:[0,0,0] cbsz:4 blgp:2
	v_mfma_scale_f32_16x16x128_f8f6f4 v[86:89], v[198:201], v[142:147], v[86:89], v240, v130 op_sel_hi:[0,0,0] cbsz:4 blgp:2
	v_mfma_scale_f32_16x16x128_f8f6f4 v[70:73], v[202:205], v[142:147], v[70:73], v240, v130 op_sel_hi:[0,0,0] cbsz:4 blgp:2
	v_mfma_scale_f32_16x16x128_f8f6f4 v[54:57], v[206:209], v[142:147], v[54:57], v240, v130 op_sel_hi:[0,0,0] cbsz:4 blgp:2
	v_mfma_scale_f32_16x16x128_f8f6f4 v[38:41], v[210:213], v[142:147], v[38:41], v240, v130 op_sel_hi:[0,0,0] cbsz:4 blgp:2
	v_mfma_scale_f32_16x16x128_f8f6f4 v[118:121], v[154:157], v[148:153], v[118:121], v240, v131 op_sel_hi:[0,0,0] cbsz:4 blgp:2
	v_mfma_scale_f32_16x16x128_f8f6f4 v[110:113], v[186:189], v[148:153], v[110:113], v240, v131 op_sel_hi:[0,0,0] cbsz:4 blgp:2
	v_mfma_scale_f32_16x16x128_f8f6f4 v[98:101], v[190:193], v[148:153], v[98:101], v240, v131 op_sel_hi:[0,0,0] cbsz:4 blgp:2
	v_mfma_scale_f32_16x16x128_f8f6f4 v[82:85], v[194:197], v[148:153], v[82:85], v240, v131 op_sel_hi:[0,0,0] cbsz:4 blgp:2
	v_mfma_scale_f32_16x16x128_f8f6f4 v[66:69], v[198:201], v[148:153], v[66:69], v240, v131 op_sel_hi:[0,0,0] cbsz:4 blgp:2
	v_mfma_scale_f32_16x16x128_f8f6f4 v[50:53], v[202:205], v[148:153], v[50:53], v240, v131 op_sel_hi:[0,0,0] cbsz:4 blgp:2
	v_mfma_scale_f32_16x16x128_f8f6f4 v[138:141], v[210:213], v[148:153], v[22:25], v240, v131 op_sel_hi:[0,0,0] cbsz:4 blgp:2
	v_mfma_scale_f32_16x16x128_f8f6f4 v[106:109], v[154:157], v[174:179], v[106:109], v240, v172 op_sel_hi:[0,0,0] cbsz:4 blgp:2
	v_mfma_scale_f32_16x16x128_f8f6f4 v[94:97], v[186:189], v[174:179], v[94:97], v240, v172 op_sel_hi:[0,0,0] cbsz:4 blgp:2
	v_mfma_scale_f32_16x16x128_f8f6f4 v[78:81], v[190:193], v[174:179], v[78:81], v240, v172 op_sel_hi:[0,0,0] cbsz:4 blgp:2
	v_mfma_scale_f32_16x16x128_f8f6f4 v[62:65], v[194:197], v[174:179], v[62:65], v240, v172 op_sel_hi:[0,0,0] cbsz:4 blgp:2
	v_mfma_scale_f32_16x16x128_f8f6f4 v[46:49], v[198:201], v[174:179], v[46:49], v240, v172 op_sel_hi:[0,0,0] cbsz:4 blgp:2
	v_mfma_scale_f32_16x16x128_f8f6f4 v[30:33], v[202:205], v[174:179], v[30:33], v240, v172 op_sel_hi:[0,0,0] cbsz:4 blgp:2
	v_mfma_scale_f32_16x16x128_f8f6f4 v[142:145], v[206:209], v[174:179], v[18:21], v240, v172 op_sel_hi:[0,0,0] cbsz:4 blgp:2
	v_mfma_scale_f32_16x16x128_f8f6f4 v[90:93], v[154:157], v[180:185], v[90:93], v240, v217 op_sel_hi:[0,0,0] cbsz:4 blgp:2
	v_mfma_scale_f32_16x16x128_f8f6f4 v[74:77], v[186:189], v[180:185], v[74:77], v240, v217 op_sel_hi:[0,0,0] cbsz:4 blgp:2
	v_mfma_scale_f32_16x16x128_f8f6f4 v[58:61], v[190:193], v[180:185], v[58:61], v240, v217 op_sel_hi:[0,0,0] cbsz:4 blgp:2
	v_mfma_scale_f32_16x16x128_f8f6f4 v[26:29], v[198:201], v[180:185], v[26:29], v240, v217 op_sel_hi:[0,0,0] cbsz:4 blgp:2
	v_mfma_scale_f32_16x16x128_f8f6f4 v[34:37], v[206:209], v[148:153], v[34:37], v240, v131 op_sel_hi:[0,0,0] cbsz:4 blgp:2
	v_mfma_scale_f32_16x16x128_f8f6f4 v[146:149], v[210:213], v[174:179], v[10:13], v240, v172 op_sel_hi:[0,0,0] cbsz:4 blgp:2
	v_mfma_scale_f32_16x16x128_f8f6f4 v[42:45], v[194:197], v[180:185], v[42:45], v240, v217 op_sel_hi:[0,0,0] cbsz:4 blgp:2
	v_mfma_scale_f32_16x16x128_f8f6f4 v[150:153], v[202:205], v[180:185], v[14:17], v240, v217 op_sel_hi:[0,0,0] cbsz:4 blgp:2
	v_mfma_scale_f32_16x16x128_f8f6f4 v[172:175], v[206:209], v[180:185], v[6:9], v240, v217 op_sel_hi:[0,0,0] cbsz:4 blgp:2
	v_mfma_scale_f32_16x16x128_f8f6f4 v[176:179], v[210:213], v[180:185], v[2:5], v240, v217 op_sel_hi:[0,0,0] cbsz:4 blgp:2
	s_barrier
	ds_read_b64 v[2:3], v167
	ds_read_b64 v[4:5], v167 offset:8
	ds_read_b64 v[6:7], v167 offset:16
	ds_read_b64 v[8:9], v170
	ds_read_b64 v[10:11], v170 offset:8
	ds_read_b64 v[12:13], v170 offset:16
	ds_read_b64 v[14:15], v169
	ds_read_b64 v[16:17], v169 offset:8
	ds_read_b64 v[18:19], v169 offset:16
	s_mov_b64 s[0:1], 0x55800
	s_mov_b32 m0, s54
	ds_read_b64 v[20:21], v168
	ds_read_b64 v[22:23], v168 offset:8
	ds_read_b64 v[24:25], v168 offset:16
	v_lshl_add_u64 v[130:131], v[132:133], 0, s[0:1]
	global_load_lds_dwordx4 v[130:131], off
	v_lshl_add_u64 v[130:131], v[134:135], 0, s[0:1]
	s_mov_b32 m0, s52
	v_lshrrev_b32_e32 v167, 8, v216
	global_load_lds_dwordx4 v[130:131], off
	v_lshl_add_u64 v[130:131], v[136:137], 0, s[0:1]
	s_mov_b32 m0, s51
	v_lshrrev_b32_e32 v168, 8, v214
	global_load_lds_dwordx4 v[130:131], off
	s_waitcnt vmcnt(3)
	s_waitcnt lgkmcnt(0)
	v_lshrrev_b32_e32 v130, 8, v171
	v_lshrrev_b32_e32 v131, 8, v215
	s_barrier
	v_mfma_scale_f32_16x16x128_f8f6f4 v[126:129], v[154:157], v[2:7], v[126:129], v240, v130 op_sel_hi:[0,0,0] cbsz:4 blgp:2
	v_mfma_scale_f32_16x16x128_f8f6f4 v[122:125], v[186:189], v[2:7], v[122:125], v240, v130 op_sel_hi:[0,0,0] cbsz:4 blgp:2
	v_mfma_scale_f32_16x16x128_f8f6f4 v[114:117], v[190:193], v[2:7], v[114:117], v240, v130 op_sel_hi:[0,0,0] cbsz:4 blgp:2
	v_mfma_scale_f32_16x16x128_f8f6f4 v[102:105], v[194:197], v[2:7], v[102:105], v240, v130 op_sel_hi:[0,0,0] cbsz:4 blgp:2
	v_mfma_scale_f32_16x16x128_f8f6f4 v[86:89], v[198:201], v[2:7], v[86:89], v240, v130 op_sel_hi:[0,0,0] cbsz:4 blgp:2
	v_mfma_scale_f32_16x16x128_f8f6f4 v[70:73], v[202:205], v[2:7], v[70:73], v240, v130 op_sel_hi:[0,0,0] cbsz:4 blgp:2
	v_mfma_scale_f32_16x16x128_f8f6f4 v[54:57], v[206:209], v[2:7], v[54:57], v240, v130 op_sel_hi:[0,0,0] cbsz:4 blgp:2
	v_mfma_scale_f32_16x16x128_f8f6f4 v[38:41], v[210:213], v[2:7], v[38:41], v240, v130 op_sel_hi:[0,0,0] cbsz:4 blgp:2
	v_mfma_scale_f32_16x16x128_f8f6f4 v[118:121], v[154:157], v[8:13], v[118:121], v240, v131 op_sel_hi:[0,0,0] cbsz:4 blgp:2
	v_mfma_scale_f32_16x16x128_f8f6f4 v[110:113], v[186:189], v[8:13], v[110:113], v240, v131 op_sel_hi:[0,0,0] cbsz:4 blgp:2
	v_mfma_scale_f32_16x16x128_f8f6f4 v[98:101], v[190:193], v[8:13], v[98:101], v240, v131 op_sel_hi:[0,0,0] cbsz:4 blgp:2
	v_mfma_scale_f32_16x16x128_f8f6f4 v[82:85], v[194:197], v[8:13], v[82:85], v240, v131 op_sel_hi:[0,0,0] cbsz:4 blgp:2
	v_mfma_scale_f32_16x16x128_f8f6f4 v[66:69], v[198:201], v[8:13], v[66:69], v240, v131 op_sel_hi:[0,0,0] cbsz:4 blgp:2
	v_mfma_scale_f32_16x16x128_f8f6f4 v[50:53], v[202:205], v[8:13], v[50:53], v240, v131 op_sel_hi:[0,0,0] cbsz:4 blgp:2
	v_mfma_scale_f32_16x16x128_f8f6f4 v[34:37], v[206:209], v[8:13], v[34:37], v240, v131 op_sel_hi:[0,0,0] cbsz:4 blgp:2
	v_mfma_scale_f32_16x16x128_f8f6f4 v[130:133], v[210:213], v[8:13], v[138:141], v240, v131 op_sel_hi:[0,0,0] cbsz:4 blgp:2
	v_mfma_scale_f32_16x16x128_f8f6f4 v[106:109], v[154:157], v[14:19], v[106:109], v240, v167 op_sel_hi:[0,0,0] cbsz:4 blgp:2
	v_mfma_scale_f32_16x16x128_f8f6f4 v[94:97], v[186:189], v[14:19], v[94:97], v240, v167 op_sel_hi:[0,0,0] cbsz:4 blgp:2
	v_mfma_scale_f32_16x16x128_f8f6f4 v[78:81], v[190:193], v[14:19], v[78:81], v240, v167 op_sel_hi:[0,0,0] cbsz:4 blgp:2
	v_mfma_scale_f32_16x16x128_f8f6f4 v[62:65], v[194:197], v[14:19], v[62:65], v240, v167 op_sel_hi:[0,0,0] cbsz:4 blgp:2
	v_mfma_scale_f32_16x16x128_f8f6f4 v[46:49], v[198:201], v[14:19], v[46:49], v240, v167 op_sel_hi:[0,0,0] cbsz:4 blgp:2
	v_mfma_scale_f32_16x16x128_f8f6f4 v[30:33], v[202:205], v[14:19], v[30:33], v240, v167 op_sel_hi:[0,0,0] cbsz:4 blgp:2
	v_mfma_scale_f32_16x16x128_f8f6f4 v[134:137], v[206:209], v[14:19], v[142:145], v240, v167 op_sel_hi:[0,0,0] cbsz:4 blgp:2
	v_mfma_scale_f32_16x16x128_f8f6f4 v[138:141], v[210:213], v[14:19], v[146:149], v240, v167 op_sel_hi:[0,0,0] cbsz:4 blgp:2
	v_mfma_scale_f32_16x16x128_f8f6f4 v[90:93], v[154:157], v[20:25], v[90:93], v240, v168 op_sel_hi:[0,0,0] cbsz:4 blgp:2
	v_mfma_scale_f32_16x16x128_f8f6f4 v[74:77], v[186:189], v[20:25], v[74:77], v240, v168 op_sel_hi:[0,0,0] cbsz:4 blgp:2
	v_mfma_scale_f32_16x16x128_f8f6f4 v[58:61], v[190:193], v[20:25], v[58:61], v240, v168 op_sel_hi:[0,0,0] cbsz:4 blgp:2
	v_mfma_scale_f32_16x16x128_f8f6f4 v[26:29], v[198:201], v[20:25], v[26:29], v240, v168 op_sel_hi:[0,0,0] cbsz:4 blgp:2
	v_mfma_scale_f32_16x16x128_f8f6f4 v[142:145], v[202:205], v[20:25], v[150:153], v240, v168 op_sel_hi:[0,0,0] cbsz:4 blgp:2
	v_mfma_scale_f32_16x16x128_f8f6f4 v[42:45], v[194:197], v[20:25], v[42:45], v240, v168 op_sel_hi:[0,0,0] cbsz:4 blgp:2
	v_mfma_scale_f32_16x16x128_f8f6f4 v[146:149], v[206:209], v[20:25], v[172:175], v240, v168 op_sel_hi:[0,0,0] cbsz:4 blgp:2
	v_mfma_scale_f32_16x16x128_f8f6f4 v[150:153], v[210:213], v[20:25], v[176:179], v240, v168 op_sel_hi:[0,0,0] cbsz:4 blgp:2
	s_barrier
	ds_read_b128 v[154:157], v166
	ds_read_b128 v[168:171], v166 offset:256
	ds_read_b128 v[172:175], v166 offset:512
	ds_read_b128 v[176:179], v166 offset:768
	ds_read_b128 v[180:183], v166 offset:1024
	ds_read_b128 v[184:187], v166 offset:1280
	ds_read_b128 v[188:191], v166 offset:1536
	ds_read_b128 v[192:195], v166 offset:1792
	ds_read_b64 v[2:3], v162
	ds_read_b64 v[4:5], v162 offset:8
	ds_read_b64 v[6:7], v162 offset:16
	ds_read_b64 v[8:9], v165
	ds_read_b64 v[10:11], v165 offset:8
	ds_read_b64 v[12:13], v165 offset:16
	ds_read_b64 v[14:15], v164
	ds_read_b64 v[16:17], v164 offset:8
	ds_read_b64 v[18:19], v164 offset:16
	ds_read_b64 v[20:21], v163
	ds_read_b64 v[22:23], v163 offset:8
	ds_read_b64 v[24:25], v163 offset:16
	v_add_u32_e32 v162, 0x21800, v161
	v_add_u32_e32 v163, 0x21820, v161
	v_add_u32_e32 v164, 0x21840, v161
	v_add_u32_e32 v161, 0x21860, v161
	ds_read_u16 v166, v162
	ds_read_u16 v167, v163
	ds_read_u16 v241, v164
	ds_read_u16 v161, v161
	s_waitcnt vmcnt(0)
	s_waitcnt lgkmcnt(0)
	s_waitcnt lgkmcnt(0)
	v_mov_b32_e32 v162, v166
	v_mov_b32_e32 v200, v167
	v_mov_b32_e32 v216, v241
	v_mov_b32_e32 v242, v161
	s_barrier
	v_mfma_scale_f32_16x16x128_f8f6f4 v[126:129], v[154:157], v[2:7], v[126:129], v240, v162 op_sel_hi:[0,0,0] cbsz:4 blgp:2
	v_mfma_scale_f32_16x16x128_f8f6f4 v[122:125], v[168:171], v[2:7], v[122:125], v240, v162 op_sel_hi:[0,0,0] cbsz:4 blgp:2
	v_mfma_scale_f32_16x16x128_f8f6f4 v[114:117], v[172:175], v[2:7], v[114:117], v240, v162 op_sel_hi:[0,0,0] cbsz:4 blgp:2
	v_mfma_scale_f32_16x16x128_f8f6f4 v[102:105], v[176:179], v[2:7], v[102:105], v240, v162 op_sel_hi:[0,0,0] cbsz:4 blgp:2
	v_mfma_scale_f32_16x16x128_f8f6f4 v[86:89], v[180:183], v[2:7], v[86:89], v240, v162 op_sel_hi:[0,0,0] cbsz:4 blgp:2
	v_mfma_scale_f32_16x16x128_f8f6f4 v[70:73], v[184:187], v[2:7], v[70:73], v240, v162 op_sel_hi:[0,0,0] cbsz:4 blgp:2
	v_mfma_scale_f32_16x16x128_f8f6f4 v[54:57], v[188:191], v[2:7], v[54:57], v240, v162 op_sel_hi:[0,0,0] cbsz:4 blgp:2
	v_mfma_scale_f32_16x16x128_f8f6f4 v[2:5], v[192:195], v[2:7], v[38:41], v240, v162 op_sel_hi:[0,0,0] cbsz:4 blgp:2
	v_mfma_scale_f32_16x16x128_f8f6f4 v[118:121], v[154:157], v[8:13], v[118:121], v240, v200 op_sel_hi:[0,0,0] cbsz:4 blgp:2
	v_mfma_scale_f32_16x16x128_f8f6f4 v[110:113], v[168:171], v[8:13], v[110:113], v240, v200 op_sel_hi:[0,0,0] cbsz:4 blgp:2
	v_mfma_scale_f32_16x16x128_f8f6f4 v[98:101], v[172:175], v[8:13], v[98:101], v240, v200 op_sel_hi:[0,0,0] cbsz:4 blgp:2
	v_mfma_scale_f32_16x16x128_f8f6f4 v[82:85], v[176:179], v[8:13], v[82:85], v240, v200 op_sel_hi:[0,0,0] cbsz:4 blgp:2
	v_mfma_scale_f32_16x16x128_f8f6f4 v[66:69], v[180:183], v[8:13], v[66:69], v240, v200 op_sel_hi:[0,0,0] cbsz:4 blgp:2
	v_mfma_scale_f32_16x16x128_f8f6f4 v[106:109], v[154:157], v[14:19], v[106:109], v240, v216 op_sel_hi:[0,0,0] cbsz:4 blgp:2
	v_mfma_scale_f32_16x16x128_f8f6f4 v[94:97], v[168:171], v[14:19], v[94:97], v240, v216 op_sel_hi:[0,0,0] cbsz:4 blgp:2
	v_mfma_scale_f32_16x16x128_f8f6f4 v[78:81], v[172:175], v[14:19], v[78:81], v240, v216 op_sel_hi:[0,0,0] cbsz:4 blgp:2
	v_mfma_scale_f32_16x16x128_f8f6f4 v[62:65], v[176:179], v[14:19], v[62:65], v240, v216 op_sel_hi:[0,0,0] cbsz:4 blgp:2
	v_mfma_scale_f32_16x16x128_f8f6f4 v[74:77], v[168:171], v[20:25], v[74:77], v240, v242 op_sel_hi:[0,0,0] cbsz:4 blgp:2
	v_mfma_scale_f32_16x16x128_f8f6f4 v[58:61], v[172:175], v[20:25], v[58:61], v240, v242 op_sel_hi:[0,0,0] cbsz:4 blgp:2
	v_mfma_scale_f32_16x16x128_f8f6f4 v[162:165], v[184:187], v[8:13], v[50:53], v240, v200 op_sel_hi:[0,0,0] cbsz:4 blgp:2
	v_mfma_scale_f32_16x16x128_f8f6f4 v[196:199], v[188:191], v[8:13], v[34:37], v240, v200 op_sel_hi:[0,0,0] cbsz:4 blgp:2
	v_mfma_scale_f32_16x16x128_f8f6f4 v[200:203], v[192:195], v[8:13], v[130:133], v240, v200 op_sel_hi:[0,0,0] cbsz:4 blgp:2
	v_mfma_scale_f32_16x16x128_f8f6f4 v[204:207], v[180:183], v[14:19], v[46:49], v240, v216 op_sel_hi:[0,0,0] cbsz:4 blgp:2
	v_mfma_scale_f32_16x16x128_f8f6f4 v[208:211], v[184:187], v[14:19], v[30:33], v240, v216 op_sel_hi:[0,0,0] cbsz:4 blgp:2
	v_mfma_scale_f32_16x16x128_f8f6f4 v[212:215], v[188:191], v[14:19], v[134:137], v240, v216 op_sel_hi:[0,0,0] cbsz:4 blgp:2
	v_mfma_scale_f32_16x16x128_f8f6f4 v[216:219], v[192:195], v[14:19], v[138:141], v240, v216 op_sel_hi:[0,0,0] cbsz:4 blgp:2
	v_mfma_scale_f32_16x16x128_f8f6f4 v[220:223], v[154:157], v[20:25], v[90:93], v240, v242 op_sel_hi:[0,0,0] cbsz:4 blgp:2
	v_mfma_scale_f32_16x16x128_f8f6f4 v[224:227], v[176:179], v[20:25], v[42:45], v240, v242 op_sel_hi:[0,0,0] cbsz:4 blgp:2
	v_mfma_scale_f32_16x16x128_f8f6f4 v[228:231], v[180:183], v[20:25], v[26:29], v240, v242 op_sel_hi:[0,0,0] cbsz:4 blgp:2
	v_mfma_scale_f32_16x16x128_f8f6f4 v[232:235], v[184:187], v[20:25], v[142:145], v240, v242 op_sel_hi:[0,0,0] cbsz:4 blgp:2
	v_mfma_scale_f32_16x16x128_f8f6f4 v[236:239], v[188:191], v[20:25], v[146:149], v240, v242 op_sel_hi:[0,0,0] cbsz:4 blgp:2
	v_mfma_scale_f32_16x16x128_f8f6f4 v[150:153], v[192:195], v[20:25], v[150:153], v240, v242 op_sel_hi:[0,0,0] cbsz:4 blgp:2
	s_barrier
	ds_read_b64 v[34:35], v1
	ds_read_b64 v[36:37], v1 offset:8
	ds_read_b64 v[38:39], v1 offset:16
	ds_read_b64 v[40:41], v160
	ds_read_b64 v[42:43], v160 offset:8
	ds_read_b64 v[44:45], v160 offset:16
	ds_read_b64 v[46:47], v159
	ds_read_b64 v[48:49], v159 offset:8
	ds_read_b64 v[50:51], v159 offset:16
	ds_read_b64 v[144:145], v158
	ds_read_b64 v[146:147], v158 offset:8
	ds_read_b64 v[148:149], v158 offset:16
	s_waitcnt lgkmcnt(0)
	v_lshrrev_b32_e32 v1, 8, v166
	v_lshrrev_b32_e32 v52, 8, v167
	v_lshrrev_b32_e32 v53, 8, v241
	v_lshrrev_b32_e32 v158, 8, v161
	s_barrier
	v_mfma_scale_f32_16x16x128_f8f6f4 v[30:33], v[154:157], v[34:39], v[126:129], v240, v1 op_sel_hi:[0,0,0] cbsz:4 blgp:2
	v_mfma_scale_f32_16x16x128_f8f6f4 v[22:25], v[168:171], v[34:39], v[122:125], v240, v1 op_sel_hi:[0,0,0] cbsz:4 blgp:2
	v_mfma_scale_f32_16x16x128_f8f6f4 v[14:17], v[172:175], v[34:39], v[114:117], v240, v1 op_sel_hi:[0,0,0] cbsz:4 blgp:2
	v_mfma_scale_f32_16x16x128_f8f6f4 v[6:9], v[176:179], v[34:39], v[102:105], v240, v1 op_sel_hi:[0,0,0] cbsz:4 blgp:2
	v_mfma_scale_f32_16x16x128_f8f6f4 v[26:29], v[180:183], v[34:39], v[86:89], v240, v1 op_sel_hi:[0,0,0] cbsz:4 blgp:2
	v_mfma_scale_f32_16x16x128_f8f6f4 v[18:21], v[184:187], v[34:39], v[70:73], v240, v1 op_sel_hi:[0,0,0] cbsz:4 blgp:2
	v_mfma_scale_f32_16x16x128_f8f6f4 v[10:13], v[188:191], v[34:39], v[54:57], v240, v1 op_sel_hi:[0,0,0] cbsz:4 blgp:2
	v_mfma_scale_f32_16x16x128_f8f6f4 v[2:5], v[192:195], v[34:39], v[2:5], v240, v1 op_sel_hi:[0,0,0] cbsz:4 blgp:2
	v_mfma_scale_f32_16x16x128_f8f6f4 v[132:135], v[154:157], v[40:45], v[118:121], v240, v52 op_sel_hi:[0,0,0] cbsz:4 blgp:2
	v_mfma_scale_f32_16x16x128_f8f6f4 v[128:131], v[168:171], v[40:45], v[110:113], v240, v52 op_sel_hi:[0,0,0] cbsz:4 blgp:2
	v_mfma_scale_f32_16x16x128_f8f6f4 v[124:127], v[172:175], v[40:45], v[98:101], v240, v52 op_sel_hi:[0,0,0] cbsz:4 blgp:2
	v_mfma_scale_f32_16x16x128_f8f6f4 v[116:119], v[176:179], v[40:45], v[82:85], v240, v52 op_sel_hi:[0,0,0] cbsz:4 blgp:2
	v_mfma_scale_f32_16x16x128_f8f6f4 v[140:143], v[180:183], v[40:45], v[66:69], v240, v52 op_sel_hi:[0,0,0] cbsz:4 blgp:2
	v_mfma_scale_f32_16x16x128_f8f6f4 v[136:139], v[184:187], v[40:45], v[162:165], v240, v52 op_sel_hi:[0,0,0] cbsz:4 blgp:2
	v_mfma_scale_f32_16x16x128_f8f6f4 v[120:123], v[188:191], v[40:45], v[196:199], v240, v52 op_sel_hi:[0,0,0] cbsz:4 blgp:2
	v_mfma_scale_f32_16x16x128_f8f6f4 v[112:115], v[192:195], v[40:45], v[200:203], v240, v52 op_sel_hi:[0,0,0] cbsz:4 blgp:2
	v_mfma_scale_f32_16x16x128_f8f6f4 v[100:103], v[154:157], v[46:51], v[106:109], v240, v53 op_sel_hi:[0,0,0] cbsz:4 blgp:2
	v_mfma_scale_f32_16x16x128_f8f6f4 v[96:99], v[168:171], v[46:51], v[94:97], v240, v53 op_sel_hi:[0,0,0] cbsz:4 blgp:2
	v_mfma_scale_f32_16x16x128_f8f6f4 v[92:95], v[172:175], v[46:51], v[78:81], v240, v53 op_sel_hi:[0,0,0] cbsz:4 blgp:2
	v_mfma_scale_f32_16x16x128_f8f6f4 v[84:87], v[176:179], v[46:51], v[62:65], v240, v53 op_sel_hi:[0,0,0] cbsz:4 blgp:2
	v_mfma_scale_f32_16x16x128_f8f6f4 v[108:111], v[180:183], v[46:51], v[204:207], v240, v53 op_sel_hi:[0,0,0] cbsz:4 blgp:2
	v_mfma_scale_f32_16x16x128_f8f6f4 v[104:107], v[184:187], v[46:51], v[208:211], v240, v53 op_sel_hi:[0,0,0] cbsz:4 blgp:2
	v_mfma_scale_f32_16x16x128_f8f6f4 v[88:91], v[188:191], v[46:51], v[212:215], v240, v53 op_sel_hi:[0,0,0] cbsz:4 blgp:2
	v_mfma_scale_f32_16x16x128_f8f6f4 v[80:83], v[192:195], v[46:51], v[216:219], v240, v53 op_sel_hi:[0,0,0] cbsz:4 blgp:2
	v_mfma_scale_f32_16x16x128_f8f6f4 v[68:71], v[154:157], v[144:149], v[220:223], v240, v158 op_sel_hi:[0,0,0] cbsz:4 blgp:2
	v_mfma_scale_f32_16x16x128_f8f6f4 v[64:67], v[168:171], v[144:149], v[74:77], v240, v158 op_sel_hi:[0,0,0] cbsz:4 blgp:2
	v_mfma_scale_f32_16x16x128_f8f6f4 v[60:63], v[172:175], v[144:149], v[58:61], v240, v158 op_sel_hi:[0,0,0] cbsz:4 blgp:2
	v_mfma_scale_f32_16x16x128_f8f6f4 v[52:55], v[176:179], v[144:149], v[224:227], v240, v158 op_sel_hi:[0,0,0] cbsz:4 blgp:2
	v_mfma_scale_f32_16x16x128_f8f6f4 v[76:79], v[180:183], v[144:149], v[228:231], v240, v158 op_sel_hi:[0,0,0] cbsz:4 blgp:2
	v_mfma_scale_f32_16x16x128_f8f6f4 v[72:75], v[184:187], v[144:149], v[232:235], v240, v158 op_sel_hi:[0,0,0] cbsz:4 blgp:2
	v_mfma_scale_f32_16x16x128_f8f6f4 v[56:59], v[188:191], v[144:149], v[236:239], v240, v158 op_sel_hi:[0,0,0] cbsz:4 blgp:2
	v_mfma_scale_f32_16x16x128_f8f6f4 v[48:51], v[192:195], v[144:149], v[150:153], v240, v158 op_sel_hi:[0,0,0] cbsz:4 blgp:2
	s_barrier
	s_cmpk_gt_u32 s33, 0xff
	s_cbranch_scc1 .LBB2_6
	s_barrier

	.amdhsa_kernel _Z6mxgemmILi0ELi1024ELi4EEvPKcS1_PKfS3_Pvi
		.amdhsa_group_segment_fixed_size 0
		.amdhsa_private_segment_fixed_size 0
		.amdhsa_kernarg_size 44
		.amdhsa_user_sgpr_count 2
		.amdhsa_user_sgpr_dispatch_ptr 0
		.amdhsa_user_sgpr_queue_ptr 0
		.amdhsa_user_sgpr_kernarg_segment_ptr 1
		.amdhsa_user_sgpr_dispatch_id 0
		.amdhsa_user_sgpr_kernarg_preload_length 0
		.amdhsa_user_sgpr_kernarg_preload_offset 0
		.amdhsa_user_sgpr_private_segment_size 0
		.amdhsa_uses_dynamic_stack 0
		.amdhsa_enable_private_segment 0
		.amdhsa_system_sgpr_workgroup_id_x 1
		.amdhsa_system_sgpr_workgroup_id_y 0
		.amdhsa_system_sgpr_workgroup_id_z 0
		.amdhsa_system_sgpr_workgroup_info 0
		.amdhsa_system_vgpr_workitem_id 0
		.amdhsa_next_free_vgpr 248
		.amdhsa_next_free_sgpr 84
		.amdhsa_accum_offset 248
		.amdhsa_reserve_vcc 1
		.amdhsa_float_round_mode_32 0
		.amdhsa_float_round_mode_16_64 0
		.amdhsa_float_denorm_mode_32 3
		.amdhsa_float_denorm_mode_16_64 3
		.amdhsa_dx10_clamp 1
		.amdhsa_ieee_mode 1
		.amdhsa_fp16_overflow 0
		.amdhsa_tg_split 0
		.amdhsa_exception_fp_ieee_invalid_op 0
		.amdhsa_exception_fp_denorm_src 0
		.amdhsa_exception_fp_ieee_div_zero 0
		.amdhsa_exception_fp_ieee_overflow 0
		.amdhsa_exception_fp_ieee_underflow 0
		.amdhsa_exception_fp_ieee_inexact 0
		.amdhsa_exception_int_div_zero 0
	.end_amdhsa_kernel

.LBB3_3:
	s_add_i32 s42, s60, 0xfffff000
	s_and_b32 s42, s42, 0x1000
	ds_read_b128 v[202:205], v175
	ds_read_b128 v[206:209], v175 offset:256
	ds_read_b128 v[210:213], v175 offset:512
	ds_read_b128 v[214:217], v175 offset:768
	ds_read_b128 v[218:221], v175 offset:1024
	ds_read_b128 v[222:225], v175 offset:1280
	ds_read_b128 v[226:229], v175 offset:1536
	ds_read_b128 v[230:233], v175 offset:1792
	ds_read_b64 v[178:179], v171
	ds_read_b64 v[180:181], v171 offset:8
	ds_read_b64 v[182:183], v171 offset:16
	ds_read_b64 v[184:185], v174
	ds_read_b64 v[186:187], v174 offset:8
	ds_read_b64 v[188:189], v174 offset:16
	ds_read_b64 v[190:191], v173
	ds_read_b64 v[192:193], v173 offset:8
	ds_read_b64 v[194:195], v173 offset:16
	s_mov_b32 m0, s57
	ds_read_b64 v[196:197], v172
	global_load_lds_dwordx4 v144, s[76:77]
	s_mov_b32 m0, s56
	ds_read_b64 v[198:199], v172 offset:8
	global_load_lds_dwordx4 v145, s[76:77]
	s_mov_b32 m0, s55
	ds_read_b64 v[200:201], v172 offset:16
	global_load_lds_dwordx4 v146, s[76:77]
	v_add_u32_e32 v152, s42, v176
	ds_read_u16 v240, v152
	ds_read_u16 v241, v152 offset:32
	ds_read_u16 v242, v152 offset:64
	s_add_i32 s42, s60, 0xfffff800
	s_and_b32 s42, s42, 0x1800
	s_add_i32 m0, s48, s42
	ds_read_u16 v243, v152 offset:96
	global_load_lds_dword v150, s[80:81]
	s_waitcnt vmcnt(6)
	s_waitcnt lgkmcnt(0)
	s_barrier
	v_mfma_scale_f32_16x16x128_f8f6f4 v[126:129], v[202:205], v[178:183], v[126:129], v177, v240 op_sel_hi:[0,0,0] cbsz:4 blgp:2
	v_mfma_scale_f32_16x16x128_f8f6f4 v[122:125], v[206:209], v[178:183], v[122:125], v177, v240 op_sel_hi:[0,0,0] cbsz:4 blgp:2
	v_mfma_scale_f32_16x16x128_f8f6f4 v[114:117], v[210:213], v[178:183], v[114:117], v177, v240 op_sel_hi:[0,0,0] cbsz:4 blgp:2
	v_mfma_scale_f32_16x16x128_f8f6f4 v[102:105], v[214:217], v[178:183], v[102:105], v177, v240 op_sel_hi:[0,0,0] cbsz:4 blgp:2
	v_mfma_scale_f32_16x16x128_f8f6f4 v[86:89], v[218:221], v[178:183], v[86:89], v177, v240 op_sel_hi:[0,0,0] cbsz:4 blgp:2
	v_mfma_scale_f32_16x16x128_f8f6f4 v[70:73], v[222:225], v[178:183], v[70:73], v177, v240 op_sel_hi:[0,0,0] cbsz:4 blgp:2
	v_mfma_scale_f32_16x16x128_f8f6f4 v[54:57], v[226:229], v[178:183], v[54:57], v177, v240 op_sel_hi:[0,0,0] cbsz:4 blgp:2
	v_mfma_scale_f32_16x16x128_f8f6f4 v[38:41], v[230:233], v[178:183], v[38:41], v177, v240 op_sel_hi:[0,0,0] cbsz:4 blgp:2
	v_mfma_scale_f32_16x16x128_f8f6f4 v[118:121], v[202:205], v[184:189], v[118:121], v177, v241 op_sel_hi:[0,0,0] cbsz:4 blgp:2
	v_mfma_scale_f32_16x16x128_f8f6f4 v[110:113], v[206:209], v[184:189], v[110:113], v177, v241 op_sel_hi:[0,0,0] cbsz:4 blgp:2
	v_mfma_scale_f32_16x16x128_f8f6f4 v[98:101], v[210:213], v[184:189], v[98:101], v177, v241 op_sel_hi:[0,0,0] cbsz:4 blgp:2
	v_mfma_scale_f32_16x16x128_f8f6f4 v[82:85], v[214:217], v[184:189], v[82:85], v177, v241 op_sel_hi:[0,0,0] cbsz:4 blgp:2
	v_mfma_scale_f32_16x16x128_f8f6f4 v[66:69], v[218:221], v[184:189], v[66:69], v177, v241 op_sel_hi:[0,0,0] cbsz:4 blgp:2
	v_mfma_scale_f32_16x16x128_f8f6f4 v[50:53], v[222:225], v[184:189], v[50:53], v177, v241 op_sel_hi:[0,0,0] cbsz:4 blgp:2
	v_mfma_scale_f32_16x16x128_f8f6f4 v[34:37], v[226:229], v[184:189], v[34:37], v177, v241 op_sel_hi:[0,0,0] cbsz:4 blgp:2
	v_mfma_scale_f32_16x16x128_f8f6f4 v[106:109], v[202:205], v[190:195], v[106:109], v177, v242 op_sel_hi:[0,0,0] cbsz:4 blgp:2
	v_mfma_scale_f32_16x16x128_f8f6f4 v[94:97], v[206:209], v[190:195], v[94:97], v177, v242 op_sel_hi:[0,0,0] cbsz:4 blgp:2
	v_mfma_scale_f32_16x16x128_f8f6f4 v[78:81], v[210:213], v[190:195], v[78:81], v177, v242 op_sel_hi:[0,0,0] cbsz:4 blgp:2
	v_mfma_scale_f32_16x16x128_f8f6f4 v[62:65], v[214:217], v[190:195], v[62:65], v177, v242 op_sel_hi:[0,0,0] cbsz:4 blgp:2
	v_mfma_scale_f32_16x16x128_f8f6f4 v[46:49], v[218:221], v[190:195], v[46:49], v177, v242 op_sel_hi:[0,0,0] cbsz:4 blgp:2
	v_mfma_scale_f32_16x16x128_f8f6f4 v[30:33], v[222:225], v[190:195], v[30:33], v177, v242 op_sel_hi:[0,0,0] cbsz:4 blgp:2
	v_mfma_scale_f32_16x16x128_f8f6f4 v[90:93], v[202:205], v[196:201], v[90:93], v177, v243 op_sel_hi:[0,0,0] cbsz:4 blgp:2
	v_mfma_scale_f32_16x16x128_f8f6f4 v[74:77], v[206:209], v[196:201], v[74:77], v177, v243 op_sel_hi:[0,0,0] cbsz:4 blgp:2
	v_mfma_scale_f32_16x16x128_f8f6f4 v[58:61], v[210:213], v[196:201], v[58:61], v177, v243 op_sel_hi:[0,0,0] cbsz:4 blgp:2
	v_mfma_scale_f32_16x16x128_f8f6f4 v[42:45], v[214:217], v[196:201], v[42:45], v177, v243 op_sel_hi:[0,0,0] cbsz:4 blgp:2
	v_mfma_scale_f32_16x16x128_f8f6f4 v[26:29], v[218:221], v[196:201], v[26:29], v177, v243 op_sel_hi:[0,0,0] cbsz:4 blgp:2
	v_mfma_scale_f32_16x16x128_f8f6f4 v[178:181], v[230:233], v[184:189], v[22:25], v177, v241 op_sel_hi:[0,0,0] cbsz:4 blgp:2
	v_mfma_scale_f32_16x16x128_f8f6f4 v[182:185], v[226:229], v[190:195], v[18:21], v177, v242 op_sel_hi:[0,0,0] cbsz:4 blgp:2
	v_mfma_scale_f32_16x16x128_f8f6f4 v[186:189], v[230:233], v[190:195], v[10:13], v177, v242 op_sel_hi:[0,0,0] cbsz:4 blgp:2
	v_mfma_scale_f32_16x16x128_f8f6f4 v[190:193], v[222:225], v[196:201], v[14:17], v177, v243 op_sel_hi:[0,0,0] cbsz:4 blgp:2
	v_mfma_scale_f32_16x16x128_f8f6f4 v[234:237], v[226:229], v[196:201], v[6:9], v177, v243 op_sel_hi:[0,0,0] cbsz:4 blgp:2
	v_mfma_scale_f32_16x16x128_f8f6f4 v[194:197], v[230:233], v[196:201], v[2:5], v177, v243 op_sel_hi:[0,0,0] cbsz:4 blgp:2
	s_barrier
	ds_read_b64 v[2:3], v167
	ds_read_b64 v[4:5], v167 offset:8
	ds_read_b64 v[6:7], v167 offset:16
	ds_read_b64 v[8:9], v170
	ds_read_b64 v[10:11], v170 offset:8
	ds_read_b64 v[12:13], v170 offset:16
	ds_read_b64 v[14:15], v169
	s_mov_b32 m0, s52
	ds_read_b64 v[16:17], v169 offset:8
	global_load_lds_dwordx4 v147, s[76:77]
	s_mov_b32 m0, s50
	ds_read_b64 v[18:19], v169 offset:16
	global_load_lds_dwordx4 v148, s[76:77]
	s_mov_b32 m0, s49
	ds_read_b64 v[20:21], v168
	global_load_lds_dwordx4 v149, s[76:77]
	s_mov_b32 m0, s13
	ds_read_b64 v[22:23], v168 offset:8
	global_load_lds_dwordx4 v142, s[72:73]
	s_mov_b32 m0, s44
	ds_read_b64 v[24:25], v168 offset:16
	global_load_lds_dwordx4 v143, s[72:73]
	s_waitcnt vmcnt(5)
	s_waitcnt lgkmcnt(0)
	s_barrier
	v_mfma_scale_f32_16x16x128_f8f6f4 v[126:129], v[202:205], v[2:7], v[126:129], v177, v240 op_sel:[0,1,0] op_sel_hi:[0,0,0] cbsz:4 blgp:2
	v_mfma_scale_f32_16x16x128_f8f6f4 v[122:125], v[206:209], v[2:7], v[122:125], v177, v240 op_sel:[0,1,0] op_sel_hi:[0,0,0] cbsz:4 blgp:2
	v_mfma_scale_f32_16x16x128_f8f6f4 v[114:117], v[210:213], v[2:7], v[114:117], v177, v240 op_sel:[0,1,0] op_sel_hi:[0,0,0] cbsz:4 blgp:2
	v_mfma_scale_f32_16x16x128_f8f6f4 v[102:105], v[214:217], v[2:7], v[102:105], v177, v240 op_sel:[0,1,0] op_sel_hi:[0,0,0] cbsz:4 blgp:2
	v_mfma_scale_f32_16x16x128_f8f6f4 v[86:89], v[218:221], v[2:7], v[86:89], v177, v240 op_sel:[0,1,0] op_sel_hi:[0,0,0] cbsz:4 blgp:2
	v_mfma_scale_f32_16x16x128_f8f6f4 v[70:73], v[222:225], v[2:7], v[70:73], v177, v240 op_sel:[0,1,0] op_sel_hi:[0,0,0] cbsz:4 blgp:2
	v_mfma_scale_f32_16x16x128_f8f6f4 v[54:57], v[226:229], v[2:7], v[54:57], v177, v240 op_sel:[0,1,0] op_sel_hi:[0,0,0] cbsz:4 blgp:2
	v_mfma_scale_f32_16x16x128_f8f6f4 v[38:41], v[230:233], v[2:7], v[38:41], v177, v240 op_sel:[0,1,0] op_sel_hi:[0,0,0] cbsz:4 blgp:2
	v_mfma_scale_f32_16x16x128_f8f6f4 v[118:121], v[202:205], v[8:13], v[118:121], v177, v241 op_sel:[0,1,0] op_sel_hi:[0,0,0] cbsz:4 blgp:2
	v_mfma_scale_f32_16x16x128_f8f6f4 v[110:113], v[206:209], v[8:13], v[110:113], v177, v241 op_sel:[0,1,0] op_sel_hi:[0,0,0] cbsz:4 blgp:2
	v_mfma_scale_f32_16x16x128_f8f6f4 v[98:101], v[210:213], v[8:13], v[98:101], v177, v241 op_sel:[0,1,0] op_sel_hi:[0,0,0] cbsz:4 blgp:2
	v_mfma_scale_f32_16x16x128_f8f6f4 v[82:85], v[214:217], v[8:13], v[82:85], v177, v241 op_sel:[0,1,0] op_sel_hi:[0,0,0] cbsz:4 blgp:2
	v_mfma_scale_f32_16x16x128_f8f6f4 v[66:69], v[218:221], v[8:13], v[66:69], v177, v241 op_sel:[0,1,0] op_sel_hi:[0,0,0] cbsz:4 blgp:2
	v_mfma_scale_f32_16x16x128_f8f6f4 v[50:53], v[222:225], v[8:13], v[50:53], v177, v241 op_sel:[0,1,0] op_sel_hi:[0,0,0] cbsz:4 blgp:2
	v_mfma_scale_f32_16x16x128_f8f6f4 v[34:37], v[226:229], v[8:13], v[34:37], v177, v241 op_sel:[0,1,0] op_sel_hi:[0,0,0] cbsz:4 blgp:2
	v_mfma_scale_f32_16x16x128_f8f6f4 v[106:109], v[202:205], v[14:19], v[106:109], v177, v242 op_sel:[0,1,0] op_sel_hi:[0,0,0] cbsz:4 blgp:2
	v_mfma_scale_f32_16x16x128_f8f6f4 v[94:97], v[206:209], v[14:19], v[94:97], v177, v242 op_sel:[0,1,0] op_sel_hi:[0,0,0] cbsz:4 blgp:2
	v_mfma_scale_f32_16x16x128_f8f6f4 v[78:81], v[210:213], v[14:19], v[78:81], v177, v242 op_sel:[0,1,0] op_sel_hi:[0,0,0] cbsz:4 blgp:2
	v_mfma_scale_f32_16x16x128_f8f6f4 v[62:65], v[214:217], v[14:19], v[62:65], v177, v242 op_sel:[0,1,0] op_sel_hi:[0,0,0] cbsz:4 blgp:2
	v_mfma_scale_f32_16x16x128_f8f6f4 v[46:49], v[218:221], v[14:19], v[46:49], v177, v242 op_sel:[0,1,0] op_sel_hi:[0,0,0] cbsz:4 blgp:2
	v_mfma_scale_f32_16x16x128_f8f6f4 v[30:33], v[222:225], v[14:19], v[30:33], v177, v242 op_sel:[0,1,0] op_sel_hi:[0,0,0] cbsz:4 blgp:2
	v_mfma_scale_f32_16x16x128_f8f6f4 v[90:93], v[202:205], v[20:25], v[90:93], v177, v243 op_sel:[0,1,0] op_sel_hi:[0,0,0] cbsz:4 blgp:2
	v_mfma_scale_f32_16x16x128_f8f6f4 v[74:77], v[206:209], v[20:25], v[74:77], v177, v243 op_sel:[0,1,0] op_sel_hi:[0,0,0] cbsz:4 blgp:2
	v_mfma_scale_f32_16x16x128_f8f6f4 v[58:61], v[210:213], v[20:25], v[58:61], v177, v243 op_sel:[0,1,0] op_sel_hi:[0,0,0] cbsz:4 blgp:2
	v_mfma_scale_f32_16x16x128_f8f6f4 v[42:45], v[214:217], v[20:25], v[42:45], v177, v243 op_sel:[0,1,0] op_sel_hi:[0,0,0] cbsz:4 blgp:2
	v_mfma_scale_f32_16x16x128_f8f6f4 v[26:29], v[218:221], v[20:25], v[26:29], v177, v243 op_sel:[0,1,0] op_sel_hi:[0,0,0] cbsz:4 blgp:2
	v_mfma_scale_f32_16x16x128_f8f6f4 v[178:181], v[230:233], v[8:13], v[178:181], v177, v241 op_sel:[0,1,0] op_sel_hi:[0,0,0] cbsz:4 blgp:2
	v_mfma_scale_f32_16x16x128_f8f6f4 v[182:185], v[226:229], v[14:19], v[182:185], v177, v242 op_sel:[0,1,0] op_sel_hi:[0,0,0] cbsz:4 blgp:2
	v_mfma_scale_f32_16x16x128_f8f6f4 v[186:189], v[230:233], v[14:19], v[186:189], v177, v242 op_sel:[0,1,0] op_sel_hi:[0,0,0] cbsz:4 blgp:2
	v_mfma_scale_f32_16x16x128_f8f6f4 v[190:193], v[222:225], v[20:25], v[190:193], v177, v243 op_sel:[0,1,0] op_sel_hi:[0,0,0] cbsz:4 blgp:2
	v_mfma_scale_f32_16x16x128_f8f6f4 v[198:201], v[226:229], v[20:25], v[234:237], v177, v243 op_sel:[0,1,0] op_sel_hi:[0,0,0] cbsz:4 blgp:2
	v_mfma_scale_f32_16x16x128_f8f6f4 v[194:197], v[230:233], v[20:25], v[194:197], v177, v243 op_sel:[0,1,0] op_sel_hi:[0,0,0] cbsz:4 blgp:2
	s_barrier
	ds_read_b128 v[202:205], v166
	ds_read_b128 v[206:209], v166 offset:256
	ds_read_b128 v[210:213], v166 offset:512
	ds_read_b128 v[214:217], v166 offset:768
	ds_read_b128 v[218:221], v166 offset:1024
	ds_read_b128 v[222:225], v166 offset:1280
	ds_read_b128 v[226:229], v166 offset:1536
	ds_read_b128 v[230:233], v166 offset:1792
	ds_read_b64 v[2:3], v162
	ds_read_b64 v[4:5], v162 offset:8
	ds_read_b64 v[6:7], v162 offset:16
	ds_read_b64 v[8:9], v165
	ds_read_b64 v[10:11], v165 offset:8
	ds_read_b64 v[12:13], v165 offset:16
	ds_read_b64 v[14:15], v164
	ds_read_b64 v[16:17], v164 offset:8
	ds_read_b64 v[18:19], v164 offset:16
	s_mov_b32 m0, s45
	ds_read_b64 v[20:21], v163
	global_load_lds_dwordx4 v144, s[78:79]
	s_mov_b32 m0, s46
	ds_read_b64 v[22:23], v163 offset:8
	global_load_lds_dwordx4 v145, s[78:79]
	s_mov_b32 m0, s47
	ds_read_b64 v[24:25], v163 offset:16
	global_load_lds_dwordx4 v146, s[78:79]
	v_add_u32_e32 v234, s42, v176
	ds_read_u16 v242, v234
	ds_read_u16 v243, v234 offset:32
	ds_read_u16 v244, v234 offset:64
	s_and_b32 s42, s60, 0x1000
	s_add_i32 m0, s48, s42
	ds_read_u16 v245, v234 offset:96
	global_load_lds_dword v151, s[80:81]
	s_waitcnt vmcnt(6)
	s_waitcnt lgkmcnt(0)
	s_barrier
	v_mfma_scale_f32_16x16x128_f8f6f4 v[126:129], v[202:205], v[2:7], v[126:129], v177, v242 op_sel_hi:[0,0,0] cbsz:4 blgp:2
	v_mfma_scale_f32_16x16x128_f8f6f4 v[122:125], v[206:209], v[2:7], v[122:125], v177, v242 op_sel_hi:[0,0,0] cbsz:4 blgp:2
	v_mfma_scale_f32_16x16x128_f8f6f4 v[114:117], v[210:213], v[2:7], v[114:117], v177, v242 op_sel_hi:[0,0,0] cbsz:4 blgp:2
	v_mfma_scale_f32_16x16x128_f8f6f4 v[102:105], v[214:217], v[2:7], v[102:105], v177, v242 op_sel_hi:[0,0,0] cbsz:4 blgp:2
	v_mfma_scale_f32_16x16x128_f8f6f4 v[86:89], v[218:221], v[2:7], v[86:89], v177, v242 op_sel_hi:[0,0,0] cbsz:4 blgp:2
	v_mfma_scale_f32_16x16x128_f8f6f4 v[70:73], v[222:225], v[2:7], v[70:73], v177, v242 op_sel_hi:[0,0,0] cbsz:4 blgp:2
	v_mfma_scale_f32_16x16x128_f8f6f4 v[54:57], v[226:229], v[2:7], v[54:57], v177, v242 op_sel_hi:[0,0,0] cbsz:4 blgp:2
	v_mfma_scale_f32_16x16x128_f8f6f4 v[38:41], v[230:233], v[2:7], v[38:41], v177, v242 op_sel_hi:[0,0,0] cbsz:4 blgp:2
	v_mfma_scale_f32_16x16x128_f8f6f4 v[118:121], v[202:205], v[8:13], v[118:121], v177, v243 op_sel_hi:[0,0,0] cbsz:4 blgp:2
	v_mfma_scale_f32_16x16x128_f8f6f4 v[110:113], v[206:209], v[8:13], v[110:113], v177, v243 op_sel_hi:[0,0,0] cbsz:4 blgp:2
	v_mfma_scale_f32_16x16x128_f8f6f4 v[98:101], v[210:213], v[8:13], v[98:101], v177, v243 op_sel_hi:[0,0,0] cbsz:4 blgp:2
	v_mfma_scale_f32_16x16x128_f8f6f4 v[82:85], v[214:217], v[8:13], v[82:85], v177, v243 op_sel_hi:[0,0,0] cbsz:4 blgp:2
	v_mfma_scale_f32_16x16x128_f8f6f4 v[66:69], v[218:221], v[8:13], v[66:69], v177, v243 op_sel_hi:[0,0,0] cbsz:4 blgp:2
	v_mfma_scale_f32_16x16x128_f8f6f4 v[50:53], v[222:225], v[8:13], v[50:53], v177, v243 op_sel_hi:[0,0,0] cbsz:4 blgp:2
	v_mfma_scale_f32_16x16x128_f8f6f4 v[34:37], v[226:229], v[8:13], v[34:37], v177, v243 op_sel_hi:[0,0,0] cbsz:4 blgp:2
	v_mfma_scale_f32_16x16x128_f8f6f4 v[106:109], v[202:205], v[14:19], v[106:109], v177, v244 op_sel_hi:[0,0,0] cbsz:4 blgp:2
	v_mfma_scale_f32_16x16x128_f8f6f4 v[94:97], v[206:209], v[14:19], v[94:97], v177, v244 op_sel_hi:[0,0,0] cbsz:4 blgp:2
	v_mfma_scale_f32_16x16x128_f8f6f4 v[78:81], v[210:213], v[14:19], v[78:81], v177, v244 op_sel_hi:[0,0,0] cbsz:4 blgp:2
	v_mfma_scale_f32_16x16x128_f8f6f4 v[62:65], v[214:217], v[14:19], v[62:65], v177, v244 op_sel_hi:[0,0,0] cbsz:4 blgp:2
	v_mfma_scale_f32_16x16x128_f8f6f4 v[46:49], v[218:221], v[14:19], v[46:49], v177, v244 op_sel_hi:[0,0,0] cbsz:4 blgp:2
	v_mfma_scale_f32_16x16x128_f8f6f4 v[30:33], v[222:225], v[14:19], v[30:33], v177, v244 op_sel_hi:[0,0,0] cbsz:4 blgp:2
	v_mfma_scale_f32_16x16x128_f8f6f4 v[238:241], v[226:229], v[14:19], v[182:185], v177, v244 op_sel_hi:[0,0,0] cbsz:4 blgp:2
	v_mfma_scale_f32_16x16x128_f8f6f4 v[14:17], v[230:233], v[14:19], v[186:189], v177, v244 op_sel_hi:[0,0,0] cbsz:4 blgp:2
	v_mfma_scale_f32_16x16x128_f8f6f4 v[90:93], v[202:205], v[20:25], v[90:93], v177, v245 op_sel_hi:[0,0,0] cbsz:4 blgp:2
	v_mfma_scale_f32_16x16x128_f8f6f4 v[74:77], v[206:209], v[20:25], v[74:77], v177, v245 op_sel_hi:[0,0,0] cbsz:4 blgp:2
	v_mfma_scale_f32_16x16x128_f8f6f4 v[58:61], v[210:213], v[20:25], v[58:61], v177, v245 op_sel_hi:[0,0,0] cbsz:4 blgp:2
	v_mfma_scale_f32_16x16x128_f8f6f4 v[42:45], v[214:217], v[20:25], v[42:45], v177, v245 op_sel_hi:[0,0,0] cbsz:4 blgp:2
	v_mfma_scale_f32_16x16x128_f8f6f4 v[26:29], v[218:221], v[20:25], v[26:29], v177, v245 op_sel_hi:[0,0,0] cbsz:4 blgp:2
	v_mfma_scale_f32_16x16x128_f8f6f4 v[234:237], v[230:233], v[8:13], v[178:181], v177, v243 op_sel_hi:[0,0,0] cbsz:4 blgp:2
	v_mfma_scale_f32_16x16x128_f8f6f4 v[190:193], v[222:225], v[20:25], v[190:193], v177, v245 op_sel_hi:[0,0,0] cbsz:4 blgp:2
	v_mfma_scale_f32_16x16x128_f8f6f4 v[198:201], v[226:229], v[20:25], v[198:201], v177, v245 op_sel_hi:[0,0,0] cbsz:4 blgp:2
	v_mfma_scale_f32_16x16x128_f8f6f4 v[194:197], v[230:233], v[20:25], v[194:197], v177, v245 op_sel_hi:[0,0,0] cbsz:4 blgp:2
	s_barrier
	ds_read_b64 v[2:3], v1
	ds_read_b64 v[4:5], v1 offset:8
	ds_read_b64 v[6:7], v1 offset:16
	ds_read_b64 v[8:9], v160
	ds_read_b64 v[10:11], v160 offset:8
	ds_read_b64 v[12:13], v160 offset:16
	ds_read_b64 v[178:179], v159
	s_mov_b32 m0, s51
	ds_read_b64 v[180:181], v159 offset:8
	global_load_lds_dwordx4 v147, s[78:79]
	s_mov_b32 m0, s53
	ds_read_b64 v[182:183], v159 offset:16
	global_load_lds_dwordx4 v148, s[78:79]
	s_mov_b32 m0, s54
	ds_read_b64 v[184:185], v158
	global_load_lds_dwordx4 v149, s[78:79]
	s_mov_b32 m0, s61
	ds_read_b64 v[186:187], v158 offset:8
	global_load_lds_dwordx4 v142, s[74:75]
	s_mov_b32 m0, s58
	ds_read_b64 v[188:189], v158 offset:16
	global_load_lds_dwordx4 v143, s[74:75]
	s_waitcnt vmcnt(5)
	s_waitcnt lgkmcnt(0)
	s_barrier
	v_mfma_scale_f32_16x16x128_f8f6f4 v[126:129], v[202:205], v[2:7], v[126:129], v177, v242 op_sel:[0,1,0] op_sel_hi:[0,0,0] cbsz:4 blgp:2
	v_mfma_scale_f32_16x16x128_f8f6f4 v[122:125], v[206:209], v[2:7], v[122:125], v177, v242 op_sel:[0,1,0] op_sel_hi:[0,0,0] cbsz:4 blgp:2
	v_mfma_scale_f32_16x16x128_f8f6f4 v[114:117], v[210:213], v[2:7], v[114:117], v177, v242 op_sel:[0,1,0] op_sel_hi:[0,0,0] cbsz:4 blgp:2
	v_mfma_scale_f32_16x16x128_f8f6f4 v[102:105], v[214:217], v[2:7], v[102:105], v177, v242 op_sel:[0,1,0] op_sel_hi:[0,0,0] cbsz:4 blgp:2
	v_mfma_scale_f32_16x16x128_f8f6f4 v[86:89], v[218:221], v[2:7], v[86:89], v177, v242 op_sel:[0,1,0] op_sel_hi:[0,0,0] cbsz:4 blgp:2
	v_mfma_scale_f32_16x16x128_f8f6f4 v[70:73], v[222:225], v[2:7], v[70:73], v177, v242 op_sel:[0,1,0] op_sel_hi:[0,0,0] cbsz:4 blgp:2
	v_mfma_scale_f32_16x16x128_f8f6f4 v[54:57], v[226:229], v[2:7], v[54:57], v177, v242 op_sel:[0,1,0] op_sel_hi:[0,0,0] cbsz:4 blgp:2
	v_mfma_scale_f32_16x16x128_f8f6f4 v[38:41], v[230:233], v[2:7], v[38:41], v177, v242 op_sel:[0,1,0] op_sel_hi:[0,0,0] cbsz:4 blgp:2
	v_mfma_scale_f32_16x16x128_f8f6f4 v[118:121], v[202:205], v[8:13], v[118:121], v177, v243 op_sel:[0,1,0] op_sel_hi:[0,0,0] cbsz:4 blgp:2
	v_mfma_scale_f32_16x16x128_f8f6f4 v[110:113], v[206:209], v[8:13], v[110:113], v177, v243 op_sel:[0,1,0] op_sel_hi:[0,0,0] cbsz:4 blgp:2
	v_mfma_scale_f32_16x16x128_f8f6f4 v[98:101], v[210:213], v[8:13], v[98:101], v177, v243 op_sel:[0,1,0] op_sel_hi:[0,0,0] cbsz:4 blgp:2
	v_mfma_scale_f32_16x16x128_f8f6f4 v[82:85], v[214:217], v[8:13], v[82:85], v177, v243 op_sel:[0,1,0] op_sel_hi:[0,0,0] cbsz:4 blgp:2
	v_mfma_scale_f32_16x16x128_f8f6f4 v[66:69], v[218:221], v[8:13], v[66:69], v177, v243 op_sel:[0,1,0] op_sel_hi:[0,0,0] cbsz:4 blgp:2
	v_mfma_scale_f32_16x16x128_f8f6f4 v[50:53], v[222:225], v[8:13], v[50:53], v177, v243 op_sel:[0,1,0] op_sel_hi:[0,0,0] cbsz:4 blgp:2
	v_mfma_scale_f32_16x16x128_f8f6f4 v[34:37], v[226:229], v[8:13], v[34:37], v177, v243 op_sel:[0,1,0] op_sel_hi:[0,0,0] cbsz:4 blgp:2
	v_mfma_scale_f32_16x16x128_f8f6f4 v[22:25], v[230:233], v[8:13], v[234:237], v177, v243 op_sel:[0,1,0] op_sel_hi:[0,0,0] cbsz:4 blgp:2
	v_mfma_scale_f32_16x16x128_f8f6f4 v[106:109], v[202:205], v[178:183], v[106:109], v177, v244 op_sel:[0,1,0] op_sel_hi:[0,0,0] cbsz:4 blgp:2
	v_mfma_scale_f32_16x16x128_f8f6f4 v[94:97], v[206:209], v[178:183], v[94:97], v177, v244 op_sel:[0,1,0] op_sel_hi:[0,0,0] cbsz:4 blgp:2
	v_mfma_scale_f32_16x16x128_f8f6f4 v[78:81], v[210:213], v[178:183], v[78:81], v177, v244 op_sel:[0,1,0] op_sel_hi:[0,0,0] cbsz:4 blgp:2
	v_mfma_scale_f32_16x16x128_f8f6f4 v[62:65], v[214:217], v[178:183], v[62:65], v177, v244 op_sel:[0,1,0] op_sel_hi:[0,0,0] cbsz:4 blgp:2
	v_mfma_scale_f32_16x16x128_f8f6f4 v[46:49], v[218:221], v[178:183], v[46:49], v177, v244 op_sel:[0,1,0] op_sel_hi:[0,0,0] cbsz:4 blgp:2
	v_mfma_scale_f32_16x16x128_f8f6f4 v[30:33], v[222:225], v[178:183], v[30:33], v177, v244 op_sel:[0,1,0] op_sel_hi:[0,0,0] cbsz:4 blgp:2
	v_mfma_scale_f32_16x16x128_f8f6f4 v[18:21], v[226:229], v[178:183], v[238:241], v177, v244 op_sel:[0,1,0] op_sel_hi:[0,0,0] cbsz:4 blgp:2
	v_mfma_scale_f32_16x16x128_f8f6f4 v[10:13], v[230:233], v[178:183], v[14:17], v177, v244 op_sel:[0,1,0] op_sel_hi:[0,0,0] cbsz:4 blgp:2
	v_mfma_scale_f32_16x16x128_f8f6f4 v[90:93], v[202:205], v[184:189], v[90:93], v177, v245 op_sel:[0,1,0] op_sel_hi:[0,0,0] cbsz:4 blgp:2
	v_mfma_scale_f32_16x16x128_f8f6f4 v[74:77], v[206:209], v[184:189], v[74:77], v177, v245 op_sel:[0,1,0] op_sel_hi:[0,0,0] cbsz:4 blgp:2
	v_mfma_scale_f32_16x16x128_f8f6f4 v[58:61], v[210:213], v[184:189], v[58:61], v177, v245 op_sel:[0,1,0] op_sel_hi:[0,0,0] cbsz:4 blgp:2
	v_mfma_scale_f32_16x16x128_f8f6f4 v[42:45], v[214:217], v[184:189], v[42:45], v177, v245 op_sel:[0,1,0] op_sel_hi:[0,0,0] cbsz:4 blgp:2
	v_mfma_scale_f32_16x16x128_f8f6f4 v[26:29], v[218:221], v[184:189], v[26:29], v177, v245 op_sel:[0,1,0] op_sel_hi:[0,0,0] cbsz:4 blgp:2
	v_mfma_scale_f32_16x16x128_f8f6f4 v[14:17], v[222:225], v[184:189], v[190:193], v177, v245 op_sel:[0,1,0] op_sel_hi:[0,0,0] cbsz:4 blgp:2
	v_mfma_scale_f32_16x16x128_f8f6f4 v[6:9], v[226:229], v[184:189], v[198:201], v177, v245 op_sel:[0,1,0] op_sel_hi:[0,0,0] cbsz:4 blgp:2
	v_mfma_scale_f32_16x16x128_f8f6f4 v[2:5], v[230:233], v[184:189], v[194:197], v177, v245 op_sel:[0,1,0] op_sel_hi:[0,0,0] cbsz:4 blgp:2
	s_barrier
	s_add_i32 s59, s59, 2
	s_addk_i32 s60, 0x1000
	s_add_u32 s72, s72, 0x8000
	s_addc_u32 s73, s73, 0
	s_add_u32 s74, s74, 0x8000
	s_addc_u32 s75, s75, 0
	s_add_u32 s76, s76, 0x18000
	s_addc_u32 s77, s77, 0
	s_add_u32 s78, s78, 0x18000
	s_addc_u32 s79, s79, 0
	s_add_u32 s80, s80, 0x1000
	s_addc_u32 s81, s81, 0
	s_cmp_lt_u32 s59, 28
	s_cbranch_scc1 .LBB3_3
	ds_read_b128 v[154:157], v175
	ds_read_b128 v[186:189], v175 offset:256
	ds_read_b128 v[190:193], v175 offset:512
	ds_read_b128 v[194:197], v175 offset:768
	ds_read_b128 v[198:201], v175 offset:1024
	ds_read_b128 v[202:205], v175 offset:1280
	ds_read_b128 v[206:209], v175 offset:1536
	ds_read_b128 v[210:213], v175 offset:1792
	ds_read_b64 v[142:143], v171
	ds_read_b64 v[144:145], v171 offset:8
	ds_read_b64 v[146:147], v171 offset:16
	ds_read_b64 v[148:149], v174
	ds_read_b64 v[150:151], v174 offset:8
	ds_read_b64 v[152:153], v174 offset:16
	ds_read_b64 v[174:175], v173
	ds_read_b64 v[176:177], v173 offset:8
	ds_read_b64 v[178:179], v173 offset:16
	ds_read_b64 v[180:181], v172
	ds_read_b64 v[182:183], v172 offset:8
	ds_read_b64 v[184:185], v172 offset:16
	v_add_u32_e32 v171, 0x21000, v248
	v_add_u32_e32 v172, 0x21020, v248
	v_add_u32_e32 v173, 0x21040, v248
	v_add_u32_e32 v214, 0x21060, v248
	s_mov_b64 s[0:1], 0x7c000
	s_mov_b32 m0, s61
	ds_read_u16 v171, v171
	ds_read_u16 v215, v172
	ds_read_u16 v216, v173
	ds_read_u16 v214, v214
	v_lshl_add_u64 v[172:173], v[138:139], 0, s[0:1]
	s_mov_b64 s[0:1], 0x7e000
	v_lshl_add_u64 v[138:139], v[138:139], 0, s[0:1]
	s_mov_b32 m0, s58
	s_mov_b64 s[0:1], 0x174000
	v_lshl_add_u64 v[138:139], v[140:141], 0, s[0:1]
	v_lshl_add_u64 v[140:141], v[138:139], 0, s[16:17]
	s_mov_b32 m0, s57
	v_lshl_add_u64 v[130:131], s[14:15], 0, v[130:131]
	global_load_lds_dwordx4 v[140:141], off
	v_lshl_add_u64 v[140:141], v[138:139], 0, s[18:19]
	s_mov_b32 m0, s56
	v_lshl_add_u64 v[138:139], v[138:139], 0, s[20:21]
	global_load_lds_dwordx4 v[140:141], off
	s_mov_b32 m0, s55
	s_mov_b64 s[0:1], 0xf800
	global_load_lds_dwordx4 v[138:139], off
	v_lshl_add_u64 v[130:131], v[130:131], 0, s[0:1]
	s_add_i32 m0, s9, 0x21800
	s_waitcnt lgkmcnt(0)
	v_mov_b32_e32 v172, v216
	global_load_lds_dword v[130:131], off
	s_waitcnt vmcnt(6)
	s_waitcnt lgkmcnt(0)
	v_mov_b32_e32 v130, v171
	v_mov_b32_e32 v131, v215
	v_mov_b32_e32 v217, v214
	s_barrier
	v_mov_b32_e32 v161, 0x7f7f7f7f
	s_nop 1
	v_mfma_scale_f32_16x16x128_f8f6f4 v[126:129], v[154:157], v[142:147], v[126:129], v161, v130 op_sel_hi:[0,0,0] cbsz:4 blgp:2
	v_mfma_scale_f32_16x16x128_f8f6f4 v[122:125], v[186:189], v[142:147], v[122:125], v161, v130 op_sel_hi:[0,0,0] cbsz:4 blgp:2
	v_mfma_scale_f32_16x16x128_f8f6f4 v[114:117], v[190:193], v[142:147], v[114:117], v161, v130 op_sel_hi:[0,0,0] cbsz:4 blgp:2
	v_mfma_scale_f32_16x16x128_f8f6f4 v[102:105], v[194:197], v[142:147], v[102:105], v161, v130 op_sel_hi:[0,0,0] cbsz:4 blgp:2
	v_mfma_scale_f32_16x16x128_f8f6f4 v[86:89], v[198:201], v[142:147], v[86:89], v161, v130 op_sel_hi:[0,0,0] cbsz:4 blgp:2
	v_mfma_scale_f32_16x16x128_f8f6f4 v[70:73], v[202:205], v[142:147], v[70:73], v161, v130 op_sel_hi:[0,0,0] cbsz:4 blgp:2
	v_mfma_scale_f32_16x16x128_f8f6f4 v[54:57], v[206:209], v[142:147], v[54:57], v161, v130 op_sel_hi:[0,0,0] cbsz:4 blgp:2
	v_mfma_scale_f32_16x16x128_f8f6f4 v[38:41], v[210:213], v[142:147], v[38:41], v161, v130 op_sel_hi:[0,0,0] cbsz:4 blgp:2
	v_mfma_scale_f32_16x16x128_f8f6f4 v[118:121], v[154:157], v[148:153], v[118:121], v161, v131 op_sel_hi:[0,0,0] cbsz:4 blgp:2
	v_mfma_scale_f32_16x16x128_f8f6f4 v[110:113], v[186:189], v[148:153], v[110:113], v161, v131 op_sel_hi:[0,0,0] cbsz:4 blgp:2
	v_mfma_scale_f32_16x16x128_f8f6f4 v[98:101], v[190:193], v[148:153], v[98:101], v161, v131 op_sel_hi:[0,0,0] cbsz:4 blgp:2
	v_mfma_scale_f32_16x16x128_f8f6f4 v[82:85], v[194:197], v[148:153], v[82:85], v161, v131 op_sel_hi:[0,0,0] cbsz:4 blgp:2
	v_mfma_scale_f32_16x16x128_f8f6f4 v[66:69], v[198:201], v[148:153], v[66:69], v161, v131 op_sel_hi:[0,0,0] cbsz:4 blgp:2
	v_mfma_scale_f32_16x16x128_f8f6f4 v[50:53], v[202:205], v[148:153], v[50:53], v161, v131 op_sel_hi:[0,0,0] cbsz:4 blgp:2
	v_mfma_scale_f32_16x16x128_f8f6f4 v[34:37], v[206:209], v[148:153], v[34:37], v161, v131 op_sel_hi:[0,0,0] cbsz:4 blgp:2
	v_mfma_scale_f32_16x16x128_f8f6f4 v[138:141], v[210:213], v[148:153], v[22:25], v161, v131 op_sel_hi:[0,0,0] cbsz:4 blgp:2
	v_mfma_scale_f32_16x16x128_f8f6f4 v[106:109], v[154:157], v[174:179], v[106:109], v161, v172 op_sel_hi:[0,0,0] cbsz:4 blgp:2
	v_mfma_scale_f32_16x16x128_f8f6f4 v[94:97], v[186:189], v[174:179], v[94:97], v161, v172 op_sel_hi:[0,0,0] cbsz:4 blgp:2
	v_mfma_scale_f32_16x16x128_f8f6f4 v[78:81], v[190:193], v[174:179], v[78:81], v161, v172 op_sel_hi:[0,0,0] cbsz:4 blgp:2
	v_mfma_scale_f32_16x16x128_f8f6f4 v[62:65], v[194:197], v[174:179], v[62:65], v161, v172 op_sel_hi:[0,0,0] cbsz:4 blgp:2
	v_mfma_scale_f32_16x16x128_f8f6f4 v[46:49], v[198:201], v[174:179], v[46:49], v161, v172 op_sel_hi:[0,0,0] cbsz:4 blgp:2
	v_mfma_scale_f32_16x16x128_f8f6f4 v[142:145], v[206:209], v[174:179], v[18:21], v161, v172 op_sel_hi:[0,0,0] cbsz:4 blgp:2
	v_mfma_scale_f32_16x16x128_f8f6f4 v[146:149], v[210:213], v[174:179], v[10:13], v161, v172 op_sel_hi:[0,0,0] cbsz:4 blgp:2
	v_mfma_scale_f32_16x16x128_f8f6f4 v[90:93], v[154:157], v[180:185], v[90:93], v161, v217 op_sel_hi:[0,0,0] cbsz:4 blgp:2
	v_mfma_scale_f32_16x16x128_f8f6f4 v[74:77], v[186:189], v[180:185], v[74:77], v161, v217 op_sel_hi:[0,0,0] cbsz:4 blgp:2
	v_mfma_scale_f32_16x16x128_f8f6f4 v[58:61], v[190:193], v[180:185], v[58:61], v161, v217 op_sel_hi:[0,0,0] cbsz:4 blgp:2
	v_mfma_scale_f32_16x16x128_f8f6f4 v[150:153], v[202:205], v[180:185], v[14:17], v161, v217 op_sel_hi:[0,0,0] cbsz:4 blgp:2
	v_mfma_scale_f32_16x16x128_f8f6f4 v[30:33], v[202:205], v[174:179], v[30:33], v161, v172 op_sel_hi:[0,0,0] cbsz:4 blgp:2
	v_mfma_scale_f32_16x16x128_f8f6f4 v[42:45], v[194:197], v[180:185], v[42:45], v161, v217 op_sel_hi:[0,0,0] cbsz:4 blgp:2
	v_mfma_scale_f32_16x16x128_f8f6f4 v[26:29], v[198:201], v[180:185], v[26:29], v161, v217 op_sel_hi:[0,0,0] cbsz:4 blgp:2
	v_mfma_scale_f32_16x16x128_f8f6f4 v[172:175], v[206:209], v[180:185], v[6:9], v161, v217 op_sel_hi:[0,0,0] cbsz:4 blgp:2
	v_mfma_scale_f32_16x16x128_f8f6f4 v[176:179], v[210:213], v[180:185], v[2:5], v161, v217 op_sel_hi:[0,0,0] cbsz:4 blgp:2
	s_barrier
	ds_read_b64 v[2:3], v167
	ds_read_b64 v[4:5], v167 offset:8
	ds_read_b64 v[6:7], v167 offset:16
	ds_read_b64 v[8:9], v170
	ds_read_b64 v[10:11], v170 offset:8
	ds_read_b64 v[12:13], v170 offset:16
	ds_read_b64 v[14:15], v169
	ds_read_b64 v[16:17], v169 offset:8
	ds_read_b64 v[18:19], v169 offset:16
	s_mov_b64 s[0:1], 0x175800
	s_mov_b32 m0, s52
	ds_read_b64 v[20:21], v168
	ds_read_b64 v[22:23], v168 offset:8
	ds_read_b64 v[24:25], v168 offset:16
	v_lshl_add_u64 v[130:131], v[132:133], 0, s[0:1]
	global_load_lds_dwordx4 v[130:131], off
	v_lshl_add_u64 v[130:131], v[134:135], 0, s[0:1]
	s_mov_b32 m0, s50
	v_lshrrev_b32_e32 v167, 8, v216
	global_load_lds_dwordx4 v[130:131], off
	v_lshl_add_u64 v[130:131], v[136:137], 0, s[0:1]
	s_mov_b32 m0, s49
	v_lshrrev_b32_e32 v168, 8, v214
	global_load_lds_dwordx4 v[130:131], off
	s_waitcnt vmcnt(3)
	s_waitcnt lgkmcnt(0)
	v_lshrrev_b32_e32 v130, 8, v171
	v_lshrrev_b32_e32 v131, 8, v215
	s_barrier
	v_mfma_scale_f32_16x16x128_f8f6f4 v[126:129], v[154:157], v[2:7], v[126:129], v161, v130 op_sel_hi:[0,0,0] cbsz:4 blgp:2
	v_mfma_scale_f32_16x16x128_f8f6f4 v[122:125], v[186:189], v[2:7], v[122:125], v161, v130 op_sel_hi:[0,0,0] cbsz:4 blgp:2
	v_mfma_scale_f32_16x16x128_f8f6f4 v[114:117], v[190:193], v[2:7], v[114:117], v161, v130 op_sel_hi:[0,0,0] cbsz:4 blgp:2
	v_mfma_scale_f32_16x16x128_f8f6f4 v[102:105], v[194:197], v[2:7], v[102:105], v161, v130 op_sel_hi:[0,0,0] cbsz:4 blgp:2
	v_mfma_scale_f32_16x16x128_f8f6f4 v[86:89], v[198:201], v[2:7], v[86:89], v161, v130 op_sel_hi:[0,0,0] cbsz:4 blgp:2
	v_mfma_scale_f32_16x16x128_f8f6f4 v[70:73], v[202:205], v[2:7], v[70:73], v161, v130 op_sel_hi:[0,0,0] cbsz:4 blgp:2
	v_mfma_scale_f32_16x16x128_f8f6f4 v[54:57], v[206:209], v[2:7], v[54:57], v161, v130 op_sel_hi:[0,0,0] cbsz:4 blgp:2
	v_mfma_scale_f32_16x16x128_f8f6f4 v[38:41], v[210:213], v[2:7], v[38:41], v161, v130 op_sel_hi:[0,0,0] cbsz:4 blgp:2
	v_mfma_scale_f32_16x16x128_f8f6f4 v[118:121], v[154:157], v[8:13], v[118:121], v161, v131 op_sel_hi:[0,0,0] cbsz:4 blgp:2
	v_mfma_scale_f32_16x16x128_f8f6f4 v[110:113], v[186:189], v[8:13], v[110:113], v161, v131 op_sel_hi:[0,0,0] cbsz:4 blgp:2
	v_mfma_scale_f32_16x16x128_f8f6f4 v[98:101], v[190:193], v[8:13], v[98:101], v161, v131 op_sel_hi:[0,0,0] cbsz:4 blgp:2
	v_mfma_scale_f32_16x16x128_f8f6f4 v[82:85], v[194:197], v[8:13], v[82:85], v161, v131 op_sel_hi:[0,0,0] cbsz:4 blgp:2
	v_mfma_scale_f32_16x16x128_f8f6f4 v[66:69], v[198:201], v[8:13], v[66:69], v161, v131 op_sel_hi:[0,0,0] cbsz:4 blgp:2
	v_mfma_scale_f32_16x16x128_f8f6f4 v[50:53], v[202:205], v[8:13], v[50:53], v161, v131 op_sel_hi:[0,0,0] cbsz:4 blgp:2
	v_mfma_scale_f32_16x16x128_f8f6f4 v[34:37], v[206:209], v[8:13], v[34:37], v161, v131 op_sel_hi:[0,0,0] cbsz:4 blgp:2
	v_mfma_scale_f32_16x16x128_f8f6f4 v[130:133], v[210:213], v[8:13], v[138:141], v161, v131 op_sel_hi:[0,0,0] cbsz:4 blgp:2
	v_mfma_scale_f32_16x16x128_f8f6f4 v[106:109], v[154:157], v[14:19], v[106:109], v161, v167 op_sel_hi:[0,0,0] cbsz:4 blgp:2
	v_mfma_scale_f32_16x16x128_f8f6f4 v[94:97], v[186:189], v[14:19], v[94:97], v161, v167 op_sel_hi:[0,0,0] cbsz:4 blgp:2
	v_mfma_scale_f32_16x16x128_f8f6f4 v[78:81], v[190:193], v[14:19], v[78:81], v161, v167 op_sel_hi:[0,0,0] cbsz:4 blgp:2
	v_mfma_scale_f32_16x16x128_f8f6f4 v[62:65], v[194:197], v[14:19], v[62:65], v161, v167 op_sel_hi:[0,0,0] cbsz:4 blgp:2
	v_mfma_scale_f32_16x16x128_f8f6f4 v[46:49], v[198:201], v[14:19], v[46:49], v161, v167 op_sel_hi:[0,0,0] cbsz:4 blgp:2
	v_mfma_scale_f32_16x16x128_f8f6f4 v[134:137], v[206:209], v[14:19], v[142:145], v161, v167 op_sel_hi:[0,0,0] cbsz:4 blgp:2
	v_mfma_scale_f32_16x16x128_f8f6f4 v[138:141], v[210:213], v[14:19], v[146:149], v161, v167 op_sel_hi:[0,0,0] cbsz:4 blgp:2
	v_mfma_scale_f32_16x16x128_f8f6f4 v[90:93], v[154:157], v[20:25], v[90:93], v161, v168 op_sel_hi:[0,0,0] cbsz:4 blgp:2
	v_mfma_scale_f32_16x16x128_f8f6f4 v[58:61], v[190:193], v[20:25], v[58:61], v161, v168 op_sel_hi:[0,0,0] cbsz:4 blgp:2
	v_mfma_scale_f32_16x16x128_f8f6f4 v[142:145], v[202:205], v[20:25], v[150:153], v161, v168 op_sel_hi:[0,0,0] cbsz:4 blgp:2
	v_mfma_scale_f32_16x16x128_f8f6f4 v[146:149], v[206:209], v[20:25], v[172:175], v161, v168 op_sel_hi:[0,0,0] cbsz:4 blgp:2
	v_mfma_scale_f32_16x16x128_f8f6f4 v[150:153], v[210:213], v[20:25], v[176:179], v161, v168 op_sel_hi:[0,0,0] cbsz:4 blgp:2
	v_mfma_scale_f32_16x16x128_f8f6f4 v[30:33], v[202:205], v[14:19], v[30:33], v161, v167 op_sel_hi:[0,0,0] cbsz:4 blgp:2
	v_mfma_scale_f32_16x16x128_f8f6f4 v[236:239], v[186:189], v[20:25], v[74:77], v161, v168 op_sel_hi:[0,0,0] cbsz:4 blgp:2
	v_mfma_scale_f32_16x16x128_f8f6f4 v[42:45], v[194:197], v[20:25], v[42:45], v161, v168 op_sel_hi:[0,0,0] cbsz:4 blgp:2
	v_mfma_scale_f32_16x16x128_f8f6f4 v[26:29], v[198:201], v[20:25], v[26:29], v161, v168 op_sel_hi:[0,0,0] cbsz:4 blgp:2
	s_barrier
	ds_read_b128 v[168:171], v166
	ds_read_b128 v[172:175], v166 offset:256
	ds_read_b128 v[176:179], v166 offset:512
	ds_read_b128 v[180:183], v166 offset:768
	ds_read_b128 v[184:187], v166 offset:1024
	ds_read_b128 v[188:191], v166 offset:1280
	ds_read_b128 v[192:195], v166 offset:1536
	ds_read_b128 v[196:199], v166 offset:1792
	ds_read_b64 v[2:3], v162
	ds_read_b64 v[4:5], v162 offset:8
	ds_read_b64 v[6:7], v162 offset:16
	ds_read_b64 v[8:9], v165
	ds_read_b64 v[10:11], v165 offset:8
	ds_read_b64 v[12:13], v165 offset:16
	ds_read_b64 v[14:15], v164
	ds_read_b64 v[16:17], v164 offset:8
	ds_read_b64 v[18:19], v164 offset:16
	ds_read_b64 v[20:21], v163
	ds_read_b64 v[22:23], v163 offset:8
	ds_read_b64 v[24:25], v163 offset:16
	v_add_u32_e32 v154, 0x21800, v248
	v_add_u32_e32 v155, 0x21820, v248
	v_add_u32_e32 v156, 0x21840, v248
	v_add_u32_e32 v157, 0x21860, v248
	ds_read_u16 v166, v154
	ds_read_u16 v167, v155
	ds_read_u16 v74, v156
	ds_read_u16 v75, v157
	s_waitcnt vmcnt(0)
	s_waitcnt lgkmcnt(0)
	s_waitcnt lgkmcnt(0)
	v_mov_b32_e32 v76, v166
	v_mov_b32_e32 v77, v167
	v_mov_b32_e32 v228, v74
	v_mov_b32_e32 v252, v75
	s_barrier
	v_mfma_scale_f32_16x16x128_f8f6f4 v[126:129], v[168:171], v[2:7], v[126:129], v161, v76 op_sel_hi:[0,0,0] cbsz:4 blgp:2
	v_mfma_scale_f32_16x16x128_f8f6f4 v[122:125], v[172:175], v[2:7], v[122:125], v161, v76 op_sel_hi:[0,0,0] cbsz:4 blgp:2
	v_mfma_scale_f32_16x16x128_f8f6f4 v[114:117], v[176:179], v[2:7], v[114:117], v161, v76 op_sel_hi:[0,0,0] cbsz:4 blgp:2
	v_mfma_scale_f32_16x16x128_f8f6f4 v[102:105], v[180:183], v[2:7], v[102:105], v161, v76 op_sel_hi:[0,0,0] cbsz:4 blgp:2
	v_mfma_scale_f32_16x16x128_f8f6f4 v[86:89], v[184:187], v[2:7], v[86:89], v161, v76 op_sel_hi:[0,0,0] cbsz:4 blgp:2
	v_mfma_scale_f32_16x16x128_f8f6f4 v[70:73], v[188:191], v[2:7], v[70:73], v161, v76 op_sel_hi:[0,0,0] cbsz:4 blgp:2
	v_mfma_scale_f32_16x16x128_f8f6f4 v[54:57], v[192:195], v[2:7], v[54:57], v161, v76 op_sel_hi:[0,0,0] cbsz:4 blgp:2
	v_mfma_scale_f32_16x16x128_f8f6f4 v[154:157], v[196:199], v[2:7], v[38:41], v161, v76 op_sel_hi:[0,0,0] cbsz:4 blgp:2
	v_mfma_scale_f32_16x16x128_f8f6f4 v[118:121], v[168:171], v[8:13], v[118:121], v161, v77 op_sel_hi:[0,0,0] cbsz:4 blgp:2
	v_mfma_scale_f32_16x16x128_f8f6f4 v[82:85], v[180:183], v[8:13], v[82:85], v161, v77 op_sel_hi:[0,0,0] cbsz:4 blgp:2
	v_mfma_scale_f32_16x16x128_f8f6f4 v[66:69], v[184:187], v[8:13], v[66:69], v161, v77 op_sel_hi:[0,0,0] cbsz:4 blgp:2
	v_mfma_scale_f32_16x16x128_f8f6f4 v[50:53], v[188:191], v[8:13], v[50:53], v161, v77 op_sel_hi:[0,0,0] cbsz:4 blgp:2
	v_mfma_scale_f32_16x16x128_f8f6f4 v[130:133], v[196:199], v[8:13], v[130:133], v161, v77 op_sel_hi:[0,0,0] cbsz:4 blgp:2
	v_mfma_scale_f32_16x16x128_f8f6f4 v[62:65], v[180:183], v[14:19], v[62:65], v161, v228 op_sel_hi:[0,0,0] cbsz:4 blgp:2
	v_mfma_scale_f32_16x16x128_f8f6f4 v[46:49], v[184:187], v[14:19], v[46:49], v161, v228 op_sel_hi:[0,0,0] cbsz:4 blgp:2
	v_mfma_scale_f32_16x16x128_f8f6f4 v[58:61], v[176:179], v[20:25], v[58:61], v161, v252 op_sel_hi:[0,0,0] cbsz:4 blgp:2
	v_mfma_scale_f32_16x16x128_f8f6f4 v[162:165], v[172:175], v[8:13], v[110:113], v161, v77 op_sel_hi:[0,0,0] cbsz:4 blgp:2
	v_mfma_scale_f32_16x16x128_f8f6f4 v[200:203], v[176:179], v[8:13], v[98:101], v161, v77 op_sel_hi:[0,0,0] cbsz:4 blgp:2
	v_mfma_scale_f32_16x16x128_f8f6f4 v[204:207], v[192:195], v[8:13], v[34:37], v161, v77 op_sel_hi:[0,0,0] cbsz:4 blgp:2
	v_mfma_scale_f32_16x16x128_f8f6f4 v[208:211], v[168:171], v[14:19], v[106:109], v161, v228 op_sel_hi:[0,0,0] cbsz:4 blgp:2
	v_mfma_scale_f32_16x16x128_f8f6f4 v[212:215], v[172:175], v[14:19], v[94:97], v161, v228 op_sel_hi:[0,0,0] cbsz:4 blgp:2
	v_mfma_scale_f32_16x16x128_f8f6f4 v[216:219], v[176:179], v[14:19], v[78:81], v161, v228 op_sel_hi:[0,0,0] cbsz:4 blgp:2
	v_mfma_scale_f32_16x16x128_f8f6f4 v[220:223], v[188:191], v[14:19], v[30:33], v161, v228 op_sel_hi:[0,0,0] cbsz:4 blgp:2
	v_mfma_scale_f32_16x16x128_f8f6f4 v[224:227], v[192:195], v[14:19], v[134:137], v161, v228 op_sel_hi:[0,0,0] cbsz:4 blgp:2
	v_mfma_scale_f32_16x16x128_f8f6f4 v[228:231], v[196:199], v[14:19], v[138:141], v161, v228 op_sel_hi:[0,0,0] cbsz:4 blgp:2
	v_mfma_scale_f32_16x16x128_f8f6f4 v[232:235], v[168:171], v[20:25], v[90:93], v161, v252 op_sel_hi:[0,0,0] cbsz:4 blgp:2
	v_mfma_scale_f32_16x16x128_f8f6f4 v[236:239], v[172:175], v[20:25], v[236:239], v161, v252 op_sel_hi:[0,0,0] cbsz:4 blgp:2
	v_mfma_scale_f32_16x16x128_f8f6f4 v[42:45], v[180:183], v[20:25], v[42:45], v161, v252 op_sel_hi:[0,0,0] cbsz:4 blgp:2
	v_mfma_scale_f32_16x16x128_f8f6f4 v[240:243], v[184:187], v[20:25], v[26:29], v161, v252 op_sel_hi:[0,0,0] cbsz:4 blgp:2
	v_mfma_scale_f32_16x16x128_f8f6f4 v[244:247], v[188:191], v[20:25], v[142:145], v161, v252 op_sel_hi:[0,0,0] cbsz:4 blgp:2
	v_mfma_scale_f32_16x16x128_f8f6f4 v[248:251], v[192:195], v[20:25], v[146:149], v161, v252 op_sel_hi:[0,0,0] cbsz:4 blgp:2
	v_mfma_scale_f32_16x16x128_f8f6f4 v[252:255], v[196:199], v[20:25], v[150:153], v161, v252 op_sel_hi:[0,0,0] cbsz:4 blgp:2
	s_barrier
	ds_read_b64 v[18:19], v1
	ds_read_b64 v[20:21], v1 offset:8
	ds_read_b64 v[22:23], v1 offset:16
	ds_read_b64 v[24:25], v160
	ds_read_b64 v[26:27], v160 offset:8
	ds_read_b64 v[28:29], v160 offset:16
	ds_read_b64 v[30:31], v159
	ds_read_b64 v[32:33], v159 offset:8
	ds_read_b64 v[34:35], v159 offset:16
	ds_read_b64 v[36:37], v158
	ds_read_b64 v[38:39], v158 offset:8
	ds_read_b64 v[40:41], v158 offset:16
	s_waitcnt lgkmcnt(0)
	v_lshrrev_b32_e32 v1, 8, v166
	v_lshrrev_b32_e32 v76, 8, v167
	v_lshrrev_b32_e32 v112, 8, v74
	v_lshrrev_b32_e32 v160, 8, v75
	s_barrier
	v_mfma_scale_f32_16x16x128_f8f6f4 v[14:17], v[168:171], v[18:23], v[126:129], v161, v1 op_sel_hi:[0,0,0] cbsz:4 blgp:2
	v_mfma_scale_f32_16x16x128_f8f6f4 v[10:13], v[172:175], v[18:23], v[122:125], v161, v1 op_sel_hi:[0,0,0] cbsz:4 blgp:2
	v_mfma_scale_f32_16x16x128_f8f6f4 v[6:9], v[176:179], v[18:23], v[114:117], v161, v1 op_sel_hi:[0,0,0] cbsz:4 blgp:2
	v_mfma_scale_f32_16x16x128_f8f6f4 v[2:5], v[180:183], v[18:23], v[102:105], v161, v1 op_sel_hi:[0,0,0] cbsz:4 blgp:2
	v_mfma_scale_f32_16x16x128_f8f6f4 v[108:111], v[184:187], v[18:23], v[86:89], v161, v1 op_sel_hi:[0,0,0] cbsz:4 blgp:2
	v_mfma_scale_f32_16x16x128_f8f6f4 v[104:107], v[188:191], v[18:23], v[70:73], v161, v1 op_sel_hi:[0,0,0] cbsz:4 blgp:2
	v_mfma_scale_f32_16x16x128_f8f6f4 v[100:103], v[192:195], v[18:23], v[54:57], v161, v1 op_sel_hi:[0,0,0] cbsz:4 blgp:2
	v_mfma_scale_f32_16x16x128_f8f6f4 v[96:99], v[196:199], v[18:23], v[154:157], v161, v1 op_sel_hi:[0,0,0] cbsz:4 blgp:2
	v_mfma_scale_f32_16x16x128_f8f6f4 v[156:159], v[168:171], v[24:29], v[118:121], v161, v76 op_sel_hi:[0,0,0] cbsz:4 blgp:2
	v_mfma_scale_f32_16x16x128_f8f6f4 v[152:155], v[172:175], v[24:29], v[162:165], v161, v76 op_sel_hi:[0,0,0] cbsz:4 blgp:2
	v_mfma_scale_f32_16x16x128_f8f6f4 v[148:151], v[176:179], v[24:29], v[200:203], v161, v76 op_sel_hi:[0,0,0] cbsz:4 blgp:2
	v_mfma_scale_f32_16x16x128_f8f6f4 v[144:147], v[180:183], v[24:29], v[82:85], v161, v76 op_sel_hi:[0,0,0] cbsz:4 blgp:2
	v_mfma_scale_f32_16x16x128_f8f6f4 v[92:95], v[184:187], v[24:29], v[66:69], v161, v76 op_sel_hi:[0,0,0] cbsz:4 blgp:2
	v_mfma_scale_f32_16x16x128_f8f6f4 v[88:91], v[188:191], v[24:29], v[50:53], v161, v76 op_sel_hi:[0,0,0] cbsz:4 blgp:2
	v_mfma_scale_f32_16x16x128_f8f6f4 v[84:87], v[192:195], v[24:29], v[204:207], v161, v76 op_sel_hi:[0,0,0] cbsz:4 blgp:2
	v_mfma_scale_f32_16x16x128_f8f6f4 v[80:83], v[196:199], v[24:29], v[130:133], v161, v76 op_sel_hi:[0,0,0] cbsz:4 blgp:2
	v_mfma_scale_f32_16x16x128_f8f6f4 v[140:143], v[168:171], v[30:35], v[208:211], v161, v112 op_sel_hi:[0,0,0] cbsz:4 blgp:2
	v_mfma_scale_f32_16x16x128_f8f6f4 v[136:139], v[172:175], v[30:35], v[212:215], v161, v112 op_sel_hi:[0,0,0] cbsz:4 blgp:2
	v_mfma_scale_f32_16x16x128_f8f6f4 v[132:135], v[176:179], v[30:35], v[216:219], v161, v112 op_sel_hi:[0,0,0] cbsz:4 blgp:2
	v_mfma_scale_f32_16x16x128_f8f6f4 v[128:131], v[180:183], v[30:35], v[62:65], v161, v112 op_sel_hi:[0,0,0] cbsz:4 blgp:2
	v_mfma_scale_f32_16x16x128_f8f6f4 v[76:79], v[184:187], v[30:35], v[46:49], v161, v112 op_sel_hi:[0,0,0] cbsz:4 blgp:2
	v_mfma_scale_f32_16x16x128_f8f6f4 v[72:75], v[188:191], v[30:35], v[220:223], v161, v112 op_sel_hi:[0,0,0] cbsz:4 blgp:2
	v_mfma_scale_f32_16x16x128_f8f6f4 v[68:71], v[192:195], v[30:35], v[224:227], v161, v112 op_sel_hi:[0,0,0] cbsz:4 blgp:2
	v_mfma_scale_f32_16x16x128_f8f6f4 v[64:67], v[196:199], v[30:35], v[228:231], v161, v112 op_sel_hi:[0,0,0] cbsz:4 blgp:2
	v_mfma_scale_f32_16x16x128_f8f6f4 v[124:127], v[168:171], v[36:41], v[232:235], v161, v160 op_sel_hi:[0,0,0] cbsz:4 blgp:2
	v_mfma_scale_f32_16x16x128_f8f6f4 v[120:123], v[172:175], v[36:41], v[236:239], v161, v160 op_sel_hi:[0,0,0] cbsz:4 blgp:2
	v_mfma_scale_f32_16x16x128_f8f6f4 v[116:119], v[176:179], v[36:41], v[58:61], v161, v160 op_sel_hi:[0,0,0] cbsz:4 blgp:2
	v_mfma_scale_f32_16x16x128_f8f6f4 v[112:115], v[180:183], v[36:41], v[42:45], v161, v160 op_sel_hi:[0,0,0] cbsz:4 blgp:2
	v_mfma_scale_f32_16x16x128_f8f6f4 v[60:63], v[184:187], v[36:41], v[240:243], v161, v160 op_sel_hi:[0,0,0] cbsz:4 blgp:2
	v_mfma_scale_f32_16x16x128_f8f6f4 v[56:59], v[188:191], v[36:41], v[244:247], v161, v160 op_sel_hi:[0,0,0] cbsz:4 blgp:2
	v_mfma_scale_f32_16x16x128_f8f6f4 v[52:55], v[192:195], v[36:41], v[248:251], v161, v160 op_sel_hi:[0,0,0] cbsz:4 blgp:2
	v_mfma_scale_f32_16x16x128_f8f6f4 v[48:51], v[196:199], v[36:41], v[252:255], v161, v160 op_sel_hi:[0,0,0] cbsz:4 blgp:2
	s_barrier
	s_cmpk_gt_u32 s33, 0xff
	s_cbranch_scc1 .LBB3_6
	s_barrier
